# v034 + mLSTM-scan normaliser loads in flight together + Fourier-fold mirrored loads issued with the main load + weight-transpose items issue 32 row loads at once + combine pass next-row prefetch
# speedup vs baseline: 1.0209x; 1.0013x over previous
; #pragma unroll 8
;     for (int i = 0; i < 32; ++i) { const int kk = 2 * i + (lane >> 5); scr[kk * 33 + (lane & 31)] = __builtin_nontemporal_load(W + (size_t)(k0 + kk) * ldw + n0 + (lane & 31)); }
; __device__ __forceinline__ void phase_p0a(const Ptrs& P, LAS unsigned char* lds, int tid_, int vcu, int G) {
;     ...
;             transpose_item(P.ple_w_gate + (size_t)l * 1024 * 1024, 1024, 64 * kb, 32 * nb, (bf16*)(P.ws + WS_PLEG) + ((size_t)l * 1024 + 32 * nb) * 1024 + 64 * kb, 1024, scr, lane); }
.LBB0_53:
	v_lshl_add_u64 v[96:97], v[50:51], 0, s[46:47]
	s_waitcnt vmcnt(15)
	v_lshl_add_u64 v[98:99], v[48:49], 0, s[46:47]
	v_lshl_add_u64 v[100:101], v[46:47], 0, s[46:47]
	s_waitcnt vmcnt(14)
	v_lshl_add_u64 v[102:103], v[44:45], 0, s[46:47]
	v_lshl_add_u64 v[104:105], v[42:43], 0, s[46:47]
	s_waitcnt vmcnt(13)
	v_lshl_add_u64 v[106:107], v[40:41], 0, s[46:47]
	v_lshl_add_u64 v[108:109], v[38:39], 0, s[46:47]
	s_waitcnt vmcnt(12)
	v_lshl_add_u64 v[110:111], v[36:37], 0, s[46:47]
	global_load_dword v134, v[96:97], off nt
	s_nop 0
	global_load_dword v135, v[98:99], off nt
	s_nop 0
	global_load_dword v136, v[100:101], off nt
	global_load_dword v137, v[102:103], off nt
	s_nop 0
	global_load_dword v138, v[104:105], off nt
	global_load_dword v139, v[106:107], off nt
	global_load_dword v140, v[108:109], off nt
	global_load_dword v141, v[110:111], off nt
	s_add_u32 s46, s46, 0x10000
	s_addc_u32 s47, s47, 0
	v_lshl_add_u64 v[96:97], v[50:51], 0, s[46:47]
	v_lshl_add_u64 v[98:99], v[48:49], 0, s[46:47]
	v_lshl_add_u64 v[100:101], v[46:47], 0, s[46:47]
	v_lshl_add_u64 v[102:103], v[44:45], 0, s[46:47]
	v_lshl_add_u64 v[104:105], v[42:43], 0, s[46:47]
	v_lshl_add_u64 v[106:107], v[40:41], 0, s[46:47]
	v_lshl_add_u64 v[108:109], v[38:39], 0, s[46:47]
	v_lshl_add_u64 v[110:111], v[36:37], 0, s[46:47]
	global_load_dword v142, v[96:97], off nt
	s_nop 0
	global_load_dword v143, v[98:99], off nt
	s_nop 0
	global_load_dword v144, v[100:101], off nt
	global_load_dword v145, v[102:103], off nt
	s_nop 0
	global_load_dword v146, v[104:105], off nt
	global_load_dword v147, v[106:107], off nt
	global_load_dword v148, v[108:109], off nt
	global_load_dword v149, v[110:111], off nt
	s_add_u32 s46, s46, 0x10000
	s_addc_u32 s47, s47, 0
	v_lshl_add_u64 v[96:97], v[50:51], 0, s[46:47]
	v_lshl_add_u64 v[98:99], v[48:49], 0, s[46:47]
	v_lshl_add_u64 v[100:101], v[46:47], 0, s[46:47]
	v_lshl_add_u64 v[102:103], v[44:45], 0, s[46:47]
	v_lshl_add_u64 v[104:105], v[42:43], 0, s[46:47]
	v_lshl_add_u64 v[106:107], v[40:41], 0, s[46:47]
	v_lshl_add_u64 v[108:109], v[38:39], 0, s[46:47]
	v_lshl_add_u64 v[110:111], v[36:37], 0, s[46:47]
	global_load_dword v150, v[96:97], off nt
	s_nop 0
	global_load_dword v151, v[98:99], off nt
	s_nop 0
	global_load_dword v152, v[100:101], off nt
	global_load_dword v153, v[102:103], off nt
	s_nop 0
	global_load_dword v154, v[104:105], off nt
	global_load_dword v155, v[106:107], off nt
	global_load_dword v156, v[108:109], off nt
	global_load_dword v157, v[110:111], off nt
	s_add_u32 s46, s46, 0x10000
	s_addc_u32 s47, s47, 0
	v_lshl_add_u64 v[96:97], v[50:51], 0, s[46:47]
	v_lshl_add_u64 v[98:99], v[48:49], 0, s[46:47]
	v_lshl_add_u64 v[100:101], v[46:47], 0, s[46:47]
	v_lshl_add_u64 v[102:103], v[44:45], 0, s[46:47]
	v_lshl_add_u64 v[104:105], v[42:43], 0, s[46:47]
	v_lshl_add_u64 v[106:107], v[40:41], 0, s[46:47]
	v_lshl_add_u64 v[108:109], v[38:39], 0, s[46:47]
	v_lshl_add_u64 v[110:111], v[36:37], 0, s[46:47]
	global_load_dword v158, v[96:97], off nt
	s_nop 0
	global_load_dword v159, v[98:99], off nt
	s_nop 0
	global_load_dword v160, v[100:101], off nt
	global_load_dword v161, v[102:103], off nt
	s_nop 0
	global_load_dword v162, v[104:105], off nt
	global_load_dword v163, v[106:107], off nt
	global_load_dword v164, v[108:109], off nt
	global_load_dword v165, v[110:111], off nt
	s_add_u32 s46, s46, 0x10000
	s_addc_u32 s47, s47, 0
	v_add_u32_e32 v104, 0x400, v35
	s_waitcnt vmcnt(30)
	ds_write2_b32 v35, v134, v135 offset1:66
	s_waitcnt vmcnt(28)
	ds_write2_b32 v35, v136, v137 offset0:132 offset1:198
	s_waitcnt vmcnt(26)
; #define LAS __attribute__((address_space(3)))
; __device__ __forceinline__ unsigned pk2(float lo, float hi) { unsigned r; asm("v_cvt_pk_bf16_f32 %0, %1, %2" : "=v"(r) : "v"(lo), "v"(hi)); return r; }
; #define LDS_FENCE() asm volatile("s_waitcnt lgkmcnt(0)" ::: "memory")
;     ...
;     for (int i = 0; i < 32; ++i) { const int kk = 2 * i + (lane >> 5); scr[kk * 33 + (lane & 31)] = __builtin_nontemporal_load(W + (size_t)(k0 + kk) * ldw + n0 + (lane & 31)); }
;     LDS_FENCE();
;     const int c = lane & 7;
; #pragma unroll
;     for (int j = 0; j < 4; ++j) { const int n = (lane >> 3) + 8 * j; const LAS float* s = scr + (8 * c) * 33 + n;
;         v4u o; o.x = pk2(s[0 * 33], s[1 * 33]); o.y = pk2(s[2 * 33], s[3 * 33]); o.z = pk2(s[4 * 33], s[5 * 33]); o.w = pk2(s[6 * 33], s[7 * 33]);
;         int nr = n;
;         if (perm16) { const int cc = (n0 + n) & 255;
;             nr = (((cc >> 3) & 1) << 7) + ((cc >> 6) << 5) + (((cc >> 4) & 3) << 3) + (cc & 7) - (n0 & 255); }
;         if (fp8) {
;             v2u o8; o8.x = (unsigned)__builtin_amdgcn_cvt_pk_fp8_f32(s[2 * 33] * SW8, s[3 * 33] * SW8, __builtin_amdgcn_cvt_pk_fp8_f32(s[0 * 33] * SW8, s[1 * 33] * SW8, 0, false), true);
;             o8.y = (unsigned)__builtin_amdgcn_cvt_pk_fp8_f32(s[6 * 33] * SW8, s[7 * 33] * SW8, __builtin_amdgcn_cvt_pk_fp8_f32(s[4 * 33] * SW8, s[5 * 33] * SW8, 0, false), true);
;             *(v2u*)((unsigned char*)dst + (ptrdiff_t)nr * Kd + 8 * c) = o8;
;         } else *(v4u*)(dst + (ptrdiff_t)nr * Kd + 8 * c) = o; }
;     LDS_FENCE();
	ds_write2_b32 v104, v138, v139 offset0:8 offset1:74
	s_waitcnt vmcnt(24)
	ds_write2_b32 v104, v140, v141 offset0:140 offset1:206
	v_add_u32_e32 v35, 0x840, v35
	v_add_u32_e32 v104, 0x400, v35
	s_waitcnt vmcnt(22)
	ds_write2_b32 v35, v142, v143 offset1:66
	s_waitcnt vmcnt(20)
	ds_write2_b32 v35, v144, v145 offset0:132 offset1:198
	s_waitcnt vmcnt(18)
	ds_write2_b32 v104, v146, v147 offset0:8 offset1:74
	s_waitcnt vmcnt(16)
	ds_write2_b32 v104, v148, v149 offset0:140 offset1:206
	v_add_u32_e32 v35, 0x840, v35
	v_add_u32_e32 v104, 0x400, v35
	s_waitcnt vmcnt(14)
	ds_write2_b32 v35, v150, v151 offset1:66
	s_waitcnt vmcnt(12)
	ds_write2_b32 v35, v152, v153 offset0:132 offset1:198
	s_waitcnt vmcnt(10)
	ds_write2_b32 v104, v154, v155 offset0:8 offset1:74
	s_waitcnt vmcnt(8)
	ds_write2_b32 v104, v156, v157 offset0:140 offset1:206
	v_add_u32_e32 v35, 0x840, v35
	v_add_u32_e32 v104, 0x400, v35
	s_waitcnt vmcnt(6)
	ds_write2_b32 v35, v158, v159 offset1:66
	s_waitcnt vmcnt(4)
	ds_write2_b32 v35, v160, v161 offset0:132 offset1:198
	s_waitcnt vmcnt(2)
	ds_write2_b32 v104, v162, v163 offset0:8 offset1:74
	s_waitcnt vmcnt(0)
	ds_write2_b32 v104, v164, v165 offset0:140 offset1:206
	v_add_u32_e32 v35, 0x840, v35
	s_cmp_lg_u32 s46, 0x40000
	v_lshlrev_b64 v[38:39], 21, v[2:3]
	s_waitcnt lgkmcnt(0)
	v_add_u32_e32 v36, 0xfffff280, v95
	v_lshl_add_u64 v[38:39], s[6:7], 0, v[38:39]
	v_lshlrev_b32_e32 v2, 11, v94
	ds_read2_b32 v[40:41], v7 offset0:33 offset1:41
	ds_read2_b32 v[42:43], v7 offset1:8
	ds_read2_b32 v[44:45], v7 offset0:66 offset1:74
	ds_read2_b32 v[46:47], v7 offset0:99 offset1:107
	ds_read2_b32 v[48:49], v7 offset0:132 offset1:140
	ds_read2_b32 v[50:51], v7 offset0:165 offset1:173
	ds_read2_b32 v[94:95], v7 offset0:198 offset1:206
	ds_read2_b32 v[96:97], v7 offset0:231 offset1:239
	v_mov_b32_e32 v37, v3
	v_lshl_add_u64 v[38:39], v[38:39], 0, v[2:3]
	v_lshl_add_u64 v[36:37], v[36:37], 1, v[38:39]
	v_lshlrev_b32_e32 v2, 1, v4
	v_lshl_add_u64 v[98:99], v[36:37], 0, v[2:3]
	v_lshlrev_b32_e32 v2, 1, v6
	v_lshl_add_u64 v[100:101], v[98:99], 0, v[2:3]
	s_waitcnt lgkmcnt(6)
	v_cvt_pk_bf16_f32 v36, v42, v40
	s_waitcnt lgkmcnt(4)
	v_cvt_pk_bf16_f32 v37, v44, v46
	s_waitcnt lgkmcnt(2)
	v_cvt_pk_bf16_f32 v38, v48, v50
	s_waitcnt lgkmcnt(0)
	v_cvt_pk_bf16_f32 v39, v94, v96
	global_store_dwordx4 v[100:101], v[36:39], off
	v_lshlrev_b32_e32 v2, 1, v8
	s_nop 0
	v_cvt_pk_bf16_f32 v36, v43, v41
	v_cvt_pk_bf16_f32 v37, v45, v47
	v_cvt_pk_bf16_f32 v38, v49, v51
	v_cvt_pk_bf16_f32 v39, v95, v97
	ds_read2_b32 v[42:43], v7 offset0:16 offset1:24
	ds_read2_b32 v[44:45], v7 offset0:49 offset1:57
	ds_read2_b32 v[46:47], v7 offset0:82 offset1:90
	ds_read2_b32 v[48:49], v7 offset0:115 offset1:123
	ds_read2_b32 v[50:51], v7 offset0:148 offset1:156
	ds_read2_b32 v[94:95], v7 offset0:181 offset1:189
	ds_read2_b32 v[96:97], v7 offset0:214 offset1:222
	ds_read2_b32 v[100:101], v7 offset0:247 offset1:255
	v_lshl_add_u64 v[40:41], v[98:99], 0, v[2:3]
	v_lshlrev_b32_e32 v2, 1, v10
	global_store_dwordx4 v[40:41], v[36:39], off
	v_lshl_add_u64 v[40:41], v[98:99], 0, v[2:3]
	v_lshlrev_b32_e32 v2, 1, v12
	s_waitcnt lgkmcnt(6)
	v_cvt_pk_bf16_f32 v36, v42, v44
	s_waitcnt lgkmcnt(4)
	v_cvt_pk_bf16_f32 v37, v46, v48
	s_waitcnt lgkmcnt(2)
	v_cvt_pk_bf16_f32 v38, v50, v94
	s_waitcnt lgkmcnt(0)
	v_cvt_pk_bf16_f32 v39, v96, v100
	global_store_dwordx4 v[40:41], v[36:39], off
	v_lshl_add_u64 v[40:41], v[98:99], 0, v[2:3]
	s_nop 0
	v_cvt_pk_bf16_f32 v36, v43, v45
	v_cvt_pk_bf16_f32 v37, v47, v49
	v_cvt_pk_bf16_f32 v38, v51, v95
	v_cvt_pk_bf16_f32 v39, v97, v101
	global_store_dwordx4 v[40:41], v[36:39], off
	s_waitcnt lgkmcnt(0)

; #pragma unroll 8
;     for (int i = 0; i < 32; ++i) { const int kk = 2 * i + (lane >> 5); scr[kk * 33 + (lane & 31)] = __builtin_nontemporal_load(W + (size_t)(k0 + kk) * ldw + n0 + (lane & 31)); }
; __device__ __forceinline__ void phase_p0a(const Ptrs& P, LAS unsigned char* lds, int tid_, int vcu, int G) {
;     ...
;             transpose_item(P.ple_w_in + (size_t)l * 256 * 1024, 1024, 64 * kb, 32 * nb, (bf16*)(P.ws + WS_PLEIN) + ((size_t)l * 1024 + 32 * nb) * 256 + 64 * kb, 256, scr, lane); continue; }
.LBB0_57:
	v_lshl_add_u64 v[96:97], v[50:51], 0, s[46:47]
	s_waitcnt vmcnt(15)
	v_lshl_add_u64 v[98:99], v[48:49], 0, s[46:47]
	v_lshl_add_u64 v[100:101], v[46:47], 0, s[46:47]
	s_waitcnt vmcnt(14)
	v_lshl_add_u64 v[102:103], v[44:45], 0, s[46:47]
	v_lshl_add_u64 v[104:105], v[42:43], 0, s[46:47]
	s_waitcnt vmcnt(13)
	v_lshl_add_u64 v[106:107], v[40:41], 0, s[46:47]
	v_lshl_add_u64 v[108:109], v[38:39], 0, s[46:47]
	s_waitcnt vmcnt(12)
	v_lshl_add_u64 v[110:111], v[36:37], 0, s[46:47]
	global_load_dword v134, v[96:97], off nt
	s_nop 0
	global_load_dword v135, v[98:99], off nt
	s_nop 0
	global_load_dword v136, v[100:101], off nt
	global_load_dword v137, v[102:103], off nt
	s_nop 0
	global_load_dword v138, v[104:105], off nt
	global_load_dword v139, v[106:107], off nt
	global_load_dword v140, v[108:109], off nt
	global_load_dword v141, v[110:111], off nt
	s_add_u32 s46, s46, 0x10000
	s_addc_u32 s47, s47, 0
	v_lshl_add_u64 v[96:97], v[50:51], 0, s[46:47]
	v_lshl_add_u64 v[98:99], v[48:49], 0, s[46:47]
	v_lshl_add_u64 v[100:101], v[46:47], 0, s[46:47]
	v_lshl_add_u64 v[102:103], v[44:45], 0, s[46:47]
	v_lshl_add_u64 v[104:105], v[42:43], 0, s[46:47]
	v_lshl_add_u64 v[106:107], v[40:41], 0, s[46:47]
	v_lshl_add_u64 v[108:109], v[38:39], 0, s[46:47]
	v_lshl_add_u64 v[110:111], v[36:37], 0, s[46:47]
	global_load_dword v142, v[96:97], off nt
	s_nop 0
	global_load_dword v143, v[98:99], off nt
	s_nop 0
	global_load_dword v144, v[100:101], off nt
	global_load_dword v145, v[102:103], off nt
	s_nop 0
	global_load_dword v146, v[104:105], off nt
	global_load_dword v147, v[106:107], off nt
	global_load_dword v148, v[108:109], off nt
	global_load_dword v149, v[110:111], off nt
	s_add_u32 s46, s46, 0x10000
	s_addc_u32 s47, s47, 0
	v_lshl_add_u64 v[96:97], v[50:51], 0, s[46:47]
	v_lshl_add_u64 v[98:99], v[48:49], 0, s[46:47]
	v_lshl_add_u64 v[100:101], v[46:47], 0, s[46:47]
	v_lshl_add_u64 v[102:103], v[44:45], 0, s[46:47]
	v_lshl_add_u64 v[104:105], v[42:43], 0, s[46:47]
	v_lshl_add_u64 v[106:107], v[40:41], 0, s[46:47]
	v_lshl_add_u64 v[108:109], v[38:39], 0, s[46:47]
	v_lshl_add_u64 v[110:111], v[36:37], 0, s[46:47]
	global_load_dword v150, v[96:97], off nt
	s_nop 0
	global_load_dword v151, v[98:99], off nt
	s_nop 0
	global_load_dword v152, v[100:101], off nt
	global_load_dword v153, v[102:103], off nt
	s_nop 0
	global_load_dword v154, v[104:105], off nt
	global_load_dword v155, v[106:107], off nt
	global_load_dword v156, v[108:109], off nt
	global_load_dword v157, v[110:111], off nt
	s_add_u32 s46, s46, 0x10000
	s_addc_u32 s47, s47, 0
	v_lshl_add_u64 v[96:97], v[50:51], 0, s[46:47]
	v_lshl_add_u64 v[98:99], v[48:49], 0, s[46:47]
	v_lshl_add_u64 v[100:101], v[46:47], 0, s[46:47]
	v_lshl_add_u64 v[102:103], v[44:45], 0, s[46:47]
	v_lshl_add_u64 v[104:105], v[42:43], 0, s[46:47]
	v_lshl_add_u64 v[106:107], v[40:41], 0, s[46:47]
	v_lshl_add_u64 v[108:109], v[38:39], 0, s[46:47]
	v_lshl_add_u64 v[110:111], v[36:37], 0, s[46:47]
	global_load_dword v158, v[96:97], off nt
	s_nop 0
	global_load_dword v159, v[98:99], off nt
	s_nop 0
	global_load_dword v160, v[100:101], off nt
	global_load_dword v161, v[102:103], off nt
	s_nop 0
	global_load_dword v162, v[104:105], off nt
	global_load_dword v163, v[106:107], off nt
	global_load_dword v164, v[108:109], off nt
	global_load_dword v165, v[110:111], off nt
	s_add_u32 s46, s46, 0x10000
	s_addc_u32 s47, s47, 0
	v_add_u32_e32 v104, 0x400, v35
	s_waitcnt vmcnt(30)
	ds_write2_b32 v35, v134, v135 offset1:66
	s_waitcnt vmcnt(28)
	ds_write2_b32 v35, v136, v137 offset0:132 offset1:198
	s_waitcnt vmcnt(26)
; #define LAS __attribute__((address_space(3)))
; __device__ __forceinline__ unsigned pk2(float lo, float hi) { unsigned r; asm("v_cvt_pk_bf16_f32 %0, %1, %2" : "=v"(r) : "v"(lo), "v"(hi)); return r; }
; #define LDS_FENCE() asm volatile("s_waitcnt lgkmcnt(0)" ::: "memory")
;     ...
;     for (int i = 0; i < 32; ++i) { const int kk = 2 * i + (lane >> 5); scr[kk * 33 + (lane & 31)] = __builtin_nontemporal_load(W + (size_t)(k0 + kk) * ldw + n0 + (lane & 31)); }
;     LDS_FENCE();
;     const int c = lane & 7;
; #pragma unroll
;     for (int j = 0; j < 4; ++j) { const int n = (lane >> 3) + 8 * j; const LAS float* s = scr + (8 * c) * 33 + n;
;         v4u o; o.x = pk2(s[0 * 33], s[1 * 33]); o.y = pk2(s[2 * 33], s[3 * 33]); o.z = pk2(s[4 * 33], s[5 * 33]); o.w = pk2(s[6 * 33], s[7 * 33]);
;         int nr = n;
;         if (perm16) { const int cc = (n0 + n) & 255;
;             nr = (((cc >> 3) & 1) << 7) + ((cc >> 6) << 5) + (((cc >> 4) & 3) << 3) + (cc & 7) - (n0 & 255); }
;         if (fp8) {
;             v2u o8; o8.x = (unsigned)__builtin_amdgcn_cvt_pk_fp8_f32(s[2 * 33] * SW8, s[3 * 33] * SW8, __builtin_amdgcn_cvt_pk_fp8_f32(s[0 * 33] * SW8, s[1 * 33] * SW8, 0, false), true);
;             o8.y = (unsigned)__builtin_amdgcn_cvt_pk_fp8_f32(s[6 * 33] * SW8, s[7 * 33] * SW8, __builtin_amdgcn_cvt_pk_fp8_f32(s[4 * 33] * SW8, s[5 * 33] * SW8, 0, false), true);
;             *(v2u*)((unsigned char*)dst + (ptrdiff_t)nr * Kd + 8 * c) = o8;
;         } else *(v4u*)(dst + (ptrdiff_t)nr * Kd + 8 * c) = o; }
;     LDS_FENCE();
	ds_write2_b32 v104, v138, v139 offset0:8 offset1:74
	s_waitcnt vmcnt(24)
	ds_write2_b32 v104, v140, v141 offset0:140 offset1:206
	v_add_u32_e32 v35, 0x840, v35
	v_add_u32_e32 v104, 0x400, v35
	s_waitcnt vmcnt(22)
	ds_write2_b32 v35, v142, v143 offset1:66
	s_waitcnt vmcnt(20)
	ds_write2_b32 v35, v144, v145 offset0:132 offset1:198
	s_waitcnt vmcnt(18)
	ds_write2_b32 v104, v146, v147 offset0:8 offset1:74
	s_waitcnt vmcnt(16)
	ds_write2_b32 v104, v148, v149 offset0:140 offset1:206
	v_add_u32_e32 v35, 0x840, v35
	v_add_u32_e32 v104, 0x400, v35
	s_waitcnt vmcnt(14)
	ds_write2_b32 v35, v150, v151 offset1:66
	s_waitcnt vmcnt(12)
	ds_write2_b32 v35, v152, v153 offset0:132 offset1:198
	s_waitcnt vmcnt(10)
	ds_write2_b32 v104, v154, v155 offset0:8 offset1:74
	s_waitcnt vmcnt(8)
	ds_write2_b32 v104, v156, v157 offset0:140 offset1:206
	v_add_u32_e32 v35, 0x840, v35
	v_add_u32_e32 v104, 0x400, v35
	s_waitcnt vmcnt(6)
	ds_write2_b32 v35, v158, v159 offset1:66
	s_waitcnt vmcnt(4)
	ds_write2_b32 v35, v160, v161 offset0:132 offset1:198
	s_waitcnt vmcnt(2)
	ds_write2_b32 v104, v162, v163 offset0:8 offset1:74
	s_waitcnt vmcnt(0)
	ds_write2_b32 v104, v164, v165 offset0:140 offset1:206
	v_add_u32_e32 v35, 0x840, v35
	s_cmp_lg_u32 s46, 0x40000
	v_lshlrev_b64 v[38:39], 19, v[2:3]
	s_waitcnt lgkmcnt(0)
	v_add_u32_e32 v36, 0xfffff380, v95
	v_lshl_add_u64 v[38:39], s[8:9], 0, v[38:39]
	v_lshlrev_b32_e32 v2, 9, v94
	ds_read2_b32 v[40:41], v7 offset0:33 offset1:41
	ds_read2_b32 v[42:43], v7 offset1:8
	ds_read2_b32 v[44:45], v7 offset0:66 offset1:74
	ds_read2_b32 v[46:47], v7 offset0:99 offset1:107
	ds_read2_b32 v[48:49], v7 offset0:132 offset1:140
	ds_read2_b32 v[50:51], v7 offset0:165 offset1:173
	ds_read2_b32 v[94:95], v7 offset0:198 offset1:206
	ds_read2_b32 v[96:97], v7 offset0:231 offset1:239
	v_mov_b32_e32 v37, v3
	v_lshl_add_u64 v[38:39], v[38:39], 0, v[2:3]
	v_lshl_add_u64 v[36:37], v[36:37], 1, v[38:39]
	v_lshlrev_b32_e32 v2, 1, v4
	v_lshl_add_u64 v[98:99], v[36:37], 0, v[2:3]
	v_lshlrev_b32_e32 v2, 1, v14
	v_lshl_add_u64 v[100:101], v[98:99], 0, v[2:3]
	s_waitcnt lgkmcnt(6)
	v_cvt_pk_bf16_f32 v36, v42, v40
	s_waitcnt lgkmcnt(4)
	v_cvt_pk_bf16_f32 v37, v44, v46
	s_waitcnt lgkmcnt(2)
	v_cvt_pk_bf16_f32 v38, v48, v50
	s_waitcnt lgkmcnt(0)
	v_cvt_pk_bf16_f32 v39, v94, v96
	global_store_dwordx4 v[100:101], v[36:39], off
	v_lshlrev_b32_e32 v2, 1, v16
	s_nop 0
	v_cvt_pk_bf16_f32 v36, v43, v41
	v_cvt_pk_bf16_f32 v37, v45, v47
	v_cvt_pk_bf16_f32 v38, v49, v51
	v_cvt_pk_bf16_f32 v39, v95, v97
	ds_read2_b32 v[42:43], v7 offset0:16 offset1:24
	ds_read2_b32 v[44:45], v7 offset0:49 offset1:57
	ds_read2_b32 v[46:47], v7 offset0:82 offset1:90
	ds_read2_b32 v[48:49], v7 offset0:115 offset1:123
	ds_read2_b32 v[50:51], v7 offset0:148 offset1:156
	ds_read2_b32 v[94:95], v7 offset0:181 offset1:189
	ds_read2_b32 v[96:97], v7 offset0:214 offset1:222
	ds_read2_b32 v[100:101], v7 offset0:247 offset1:255
	v_lshl_add_u64 v[40:41], v[98:99], 0, v[2:3]
	v_lshlrev_b32_e32 v2, 1, v18
	global_store_dwordx4 v[40:41], v[36:39], off
	v_lshl_add_u64 v[40:41], v[98:99], 0, v[2:3]
	v_lshlrev_b32_e32 v2, 1, v20
	s_waitcnt lgkmcnt(6)
	v_cvt_pk_bf16_f32 v36, v42, v44
	s_waitcnt lgkmcnt(4)
	v_cvt_pk_bf16_f32 v37, v46, v48
	s_waitcnt lgkmcnt(2)
	v_cvt_pk_bf16_f32 v38, v50, v94
	s_waitcnt lgkmcnt(0)
	v_cvt_pk_bf16_f32 v39, v96, v100
	global_store_dwordx4 v[40:41], v[36:39], off
	v_lshl_add_u64 v[40:41], v[98:99], 0, v[2:3]
	s_nop 0
	v_cvt_pk_bf16_f32 v36, v43, v45
	v_cvt_pk_bf16_f32 v37, v47, v49
	v_cvt_pk_bf16_f32 v38, v51, v95
	v_cvt_pk_bf16_f32 v39, v97, v101
	global_store_dwordx4 v[40:41], v[36:39], off
	s_waitcnt lgkmcnt(0)

; #pragma unroll 8
;     for (int i = 0; i < 32; ++i) { const int kk = 2 * i + (lane >> 5); scr[kk * 33 + (lane & 31)] = __builtin_nontemporal_load(W + (size_t)(k0 + kk) * ldw + n0 + (lane & 31)); }
; __device__ __forceinline__ void phase_p0a(const Ptrs& P, LAS unsigned char* lds, int tid_, int vcu, int G) {
;     ...
;             transpose_item(P.router_w + (size_t)l * 1024 * 128, 128, 64 * kb, 32 * nb, (bf16*)(P.ws + WS_RS + (size_t)l * RS_L) + ((size_t)32 * nb) * 1024 + 64 * kb, 1024, scr, lane); continue; }
.LBB0_62:
	v_lshl_add_u64 v[96:97], v[50:51], 0, s[44:45]
	s_waitcnt vmcnt(15)
	v_lshl_add_u64 v[98:99], v[48:49], 0, s[44:45]
	v_lshl_add_u64 v[100:101], v[46:47], 0, s[44:45]
	s_waitcnt vmcnt(14)
	v_lshl_add_u64 v[102:103], v[44:45], 0, s[44:45]
	v_lshl_add_u64 v[104:105], v[42:43], 0, s[44:45]
	s_waitcnt vmcnt(13)
	v_lshl_add_u64 v[106:107], v[40:41], 0, s[44:45]
	v_lshl_add_u64 v[108:109], v[38:39], 0, s[44:45]
	s_waitcnt vmcnt(12)
	v_lshl_add_u64 v[110:111], v[36:37], 0, s[44:45]
	global_load_dword v134, v[96:97], off nt
	s_nop 0
	global_load_dword v135, v[98:99], off nt
	s_nop 0
	global_load_dword v136, v[100:101], off nt
	global_load_dword v137, v[102:103], off nt
	s_nop 0
	global_load_dword v138, v[104:105], off nt
	global_load_dword v139, v[106:107], off nt
	global_load_dword v140, v[108:109], off nt
	global_load_dword v141, v[110:111], off nt
	s_add_u32 s44, s44, 0x2000
	s_addc_u32 s45, s45, 0
	v_lshl_add_u64 v[96:97], v[50:51], 0, s[44:45]
	v_lshl_add_u64 v[98:99], v[48:49], 0, s[44:45]
	v_lshl_add_u64 v[100:101], v[46:47], 0, s[44:45]
	v_lshl_add_u64 v[102:103], v[44:45], 0, s[44:45]
	v_lshl_add_u64 v[104:105], v[42:43], 0, s[44:45]
	v_lshl_add_u64 v[106:107], v[40:41], 0, s[44:45]
	v_lshl_add_u64 v[108:109], v[38:39], 0, s[44:45]
	v_lshl_add_u64 v[110:111], v[36:37], 0, s[44:45]
	global_load_dword v142, v[96:97], off nt
	s_nop 0
	global_load_dword v143, v[98:99], off nt
	s_nop 0
	global_load_dword v144, v[100:101], off nt
	global_load_dword v145, v[102:103], off nt
	s_nop 0
	global_load_dword v146, v[104:105], off nt
	global_load_dword v147, v[106:107], off nt
	global_load_dword v148, v[108:109], off nt
	global_load_dword v149, v[110:111], off nt
	s_add_u32 s44, s44, 0x2000
	s_addc_u32 s45, s45, 0
	v_lshl_add_u64 v[96:97], v[50:51], 0, s[44:45]
	v_lshl_add_u64 v[98:99], v[48:49], 0, s[44:45]
	v_lshl_add_u64 v[100:101], v[46:47], 0, s[44:45]
	v_lshl_add_u64 v[102:103], v[44:45], 0, s[44:45]
	v_lshl_add_u64 v[104:105], v[42:43], 0, s[44:45]
	v_lshl_add_u64 v[106:107], v[40:41], 0, s[44:45]
	v_lshl_add_u64 v[108:109], v[38:39], 0, s[44:45]
	v_lshl_add_u64 v[110:111], v[36:37], 0, s[44:45]
	global_load_dword v150, v[96:97], off nt
	s_nop 0
	global_load_dword v151, v[98:99], off nt
	s_nop 0
	global_load_dword v152, v[100:101], off nt
	global_load_dword v153, v[102:103], off nt
	s_nop 0
	global_load_dword v154, v[104:105], off nt
	global_load_dword v155, v[106:107], off nt
	global_load_dword v156, v[108:109], off nt
	global_load_dword v157, v[110:111], off nt
	s_add_u32 s44, s44, 0x2000
	s_addc_u32 s45, s45, 0
	v_lshl_add_u64 v[96:97], v[50:51], 0, s[44:45]
	v_lshl_add_u64 v[98:99], v[48:49], 0, s[44:45]
	v_lshl_add_u64 v[100:101], v[46:47], 0, s[44:45]
	v_lshl_add_u64 v[102:103], v[44:45], 0, s[44:45]
	v_lshl_add_u64 v[104:105], v[42:43], 0, s[44:45]
	v_lshl_add_u64 v[106:107], v[40:41], 0, s[44:45]
	v_lshl_add_u64 v[108:109], v[38:39], 0, s[44:45]
	v_lshl_add_u64 v[110:111], v[36:37], 0, s[44:45]
	global_load_dword v158, v[96:97], off nt
	s_nop 0
	global_load_dword v159, v[98:99], off nt
	s_nop 0
	global_load_dword v160, v[100:101], off nt
	global_load_dword v161, v[102:103], off nt
	s_nop 0
	global_load_dword v162, v[104:105], off nt
	global_load_dword v163, v[106:107], off nt
	global_load_dword v164, v[108:109], off nt
	global_load_dword v165, v[110:111], off nt
	s_add_u32 s44, s44, 0x2000
	s_addc_u32 s45, s45, 0
	v_add_u32_e32 v104, 0x400, v95
	s_waitcnt vmcnt(30)
	ds_write2_b32 v95, v134, v135 offset1:66
	s_waitcnt vmcnt(28)
	ds_write2_b32 v95, v136, v137 offset0:132 offset1:198
	s_waitcnt vmcnt(26)
	ds_write2_b32 v104, v138, v139 offset0:8 offset1:74
	s_waitcnt vmcnt(24)
; #define LAS __attribute__((address_space(3)))
; __device__ __forceinline__ unsigned pk2(float lo, float hi) { unsigned r; asm("v_cvt_pk_bf16_f32 %0, %1, %2" : "=v"(r) : "v"(lo), "v"(hi)); return r; }
; #define LDS_FENCE() asm volatile("s_waitcnt lgkmcnt(0)" ::: "memory")
;     ...
;     for (int i = 0; i < 32; ++i) { const int kk = 2 * i + (lane >> 5); scr[kk * 33 + (lane & 31)] = __builtin_nontemporal_load(W + (size_t)(k0 + kk) * ldw + n0 + (lane & 31)); }
;     LDS_FENCE();
;     const int c = lane & 7;
; #pragma unroll
;     for (int j = 0; j < 4; ++j) { const int n = (lane >> 3) + 8 * j; const LAS float* s = scr + (8 * c) * 33 + n;
;         v4u o; o.x = pk2(s[0 * 33], s[1 * 33]); o.y = pk2(s[2 * 33], s[3 * 33]); o.z = pk2(s[4 * 33], s[5 * 33]); o.w = pk2(s[6 * 33], s[7 * 33]);
;         int nr = n;
;         if (perm16) { const int cc = (n0 + n) & 255;
;             nr = (((cc >> 3) & 1) << 7) + ((cc >> 6) << 5) + (((cc >> 4) & 3) << 3) + (cc & 7) - (n0 & 255); }
;         if (fp8) {
;             v2u o8; o8.x = (unsigned)__builtin_amdgcn_cvt_pk_fp8_f32(s[2 * 33] * SW8, s[3 * 33] * SW8, __builtin_amdgcn_cvt_pk_fp8_f32(s[0 * 33] * SW8, s[1 * 33] * SW8, 0, false), true);
;             o8.y = (unsigned)__builtin_amdgcn_cvt_pk_fp8_f32(s[6 * 33] * SW8, s[7 * 33] * SW8, __builtin_amdgcn_cvt_pk_fp8_f32(s[4 * 33] * SW8, s[5 * 33] * SW8, 0, false), true);
;             *(v2u*)((unsigned char*)dst + (ptrdiff_t)nr * Kd + 8 * c) = o8;
;         } else *(v4u*)(dst + (ptrdiff_t)nr * Kd + 8 * c) = o; }
;     LDS_FENCE();
	ds_write2_b32 v104, v140, v141 offset0:140 offset1:206
	v_add_u32_e32 v95, 0x840, v95
	v_add_u32_e32 v104, 0x400, v95
	s_waitcnt vmcnt(22)
	ds_write2_b32 v95, v142, v143 offset1:66
	s_waitcnt vmcnt(20)
	ds_write2_b32 v95, v144, v145 offset0:132 offset1:198
	s_waitcnt vmcnt(18)
	ds_write2_b32 v104, v146, v147 offset0:8 offset1:74
	s_waitcnt vmcnt(16)
	ds_write2_b32 v104, v148, v149 offset0:140 offset1:206
	v_add_u32_e32 v95, 0x840, v95
	v_add_u32_e32 v104, 0x400, v95
	s_waitcnt vmcnt(14)
	ds_write2_b32 v95, v150, v151 offset1:66
	s_waitcnt vmcnt(12)
	ds_write2_b32 v95, v152, v153 offset0:132 offset1:198
	s_waitcnt vmcnt(10)
	ds_write2_b32 v104, v154, v155 offset0:8 offset1:74
	s_waitcnt vmcnt(8)
	ds_write2_b32 v104, v156, v157 offset0:140 offset1:206
	v_add_u32_e32 v95, 0x840, v95
	v_add_u32_e32 v104, 0x400, v95
	s_waitcnt vmcnt(6)
	ds_write2_b32 v95, v158, v159 offset1:66
	s_waitcnt vmcnt(4)
	ds_write2_b32 v95, v160, v161 offset0:132 offset1:198
	s_waitcnt vmcnt(2)
	ds_write2_b32 v104, v162, v163 offset0:8 offset1:74
	s_waitcnt vmcnt(0)
	ds_write2_b32 v104, v164, v165 offset0:140 offset1:206
	v_add_u32_e32 v95, 0x840, v95
	s_cmpk_lg_u32 s44, 0x8000
	v_mov_b64_e32 v[40:41], s[10:11]
	v_and_b32_sdwa v36, v35, v93 dst_sel:WORD_1 dst_unused:UNUSED_PAD src0_sel:DWORD src1_sel:DWORD
	v_mad_u64_u32 v[40:41], s[44:45], v2, s55, v[40:41]
	v_mov_b32_e32 v37, v3
	s_waitcnt lgkmcnt(0)
	v_add_u32_e32 v38, 0xffffa000, v94
	v_lshl_add_u64 v[36:37], v[40:41], 0, v[36:37]
	ds_read2_b32 v[40:41], v7 offset0:33 offset1:41
	ds_read2_b32 v[42:43], v7 offset1:8
	ds_read2_b32 v[44:45], v7 offset0:66 offset1:74
	ds_read2_b32 v[46:47], v7 offset0:99 offset1:107
	ds_read2_b32 v[48:49], v7 offset0:132 offset1:140
	ds_read2_b32 v[50:51], v7 offset0:165 offset1:173
	ds_read2_b32 v[94:95], v7 offset0:198 offset1:206
	ds_read2_b32 v[96:97], v7 offset0:231 offset1:239
	v_mov_b32_e32 v39, v3
	v_lshl_add_u64 v[36:37], v[38:39], 1, v[36:37]
	v_lshlrev_b32_e32 v2, 1, v4
	v_lshl_add_u64 v[98:99], v[36:37], 0, v[2:3]
	v_lshlrev_b32_e32 v2, 1, v6
	v_lshl_add_u64 v[100:101], v[98:99], 0, v[2:3]
	s_waitcnt lgkmcnt(6)
	v_cvt_pk_bf16_f32 v36, v42, v40
	s_waitcnt lgkmcnt(4)
	v_cvt_pk_bf16_f32 v37, v44, v46
	s_waitcnt lgkmcnt(2)
	v_cvt_pk_bf16_f32 v38, v48, v50
	s_waitcnt lgkmcnt(0)
	v_cvt_pk_bf16_f32 v39, v94, v96
	global_store_dwordx4 v[100:101], v[36:39], off
	v_lshlrev_b32_e32 v2, 1, v8
	s_nop 0
	v_cvt_pk_bf16_f32 v36, v43, v41
	v_cvt_pk_bf16_f32 v37, v45, v47
	v_cvt_pk_bf16_f32 v38, v49, v51
	v_cvt_pk_bf16_f32 v39, v95, v97
	ds_read2_b32 v[42:43], v7 offset0:16 offset1:24
	ds_read2_b32 v[44:45], v7 offset0:49 offset1:57
	ds_read2_b32 v[46:47], v7 offset0:82 offset1:90
	ds_read2_b32 v[48:49], v7 offset0:115 offset1:123
	ds_read2_b32 v[50:51], v7 offset0:148 offset1:156
	ds_read2_b32 v[94:95], v7 offset0:181 offset1:189
	ds_read2_b32 v[96:97], v7 offset0:214 offset1:222
	ds_read2_b32 v[100:101], v7 offset0:247 offset1:255
	v_lshl_add_u64 v[40:41], v[98:99], 0, v[2:3]
	v_lshlrev_b32_e32 v2, 1, v10
	global_store_dwordx4 v[40:41], v[36:39], off
	v_lshl_add_u64 v[40:41], v[98:99], 0, v[2:3]
	v_lshlrev_b32_e32 v2, 1, v12
	s_waitcnt lgkmcnt(6)
	v_cvt_pk_bf16_f32 v36, v42, v44
	s_waitcnt lgkmcnt(4)
	v_cvt_pk_bf16_f32 v37, v46, v48
	s_waitcnt lgkmcnt(2)
	v_cvt_pk_bf16_f32 v38, v50, v94
	s_waitcnt lgkmcnt(0)
	v_cvt_pk_bf16_f32 v39, v96, v100
	global_store_dwordx4 v[40:41], v[36:39], off
	v_lshl_add_u64 v[40:41], v[98:99], 0, v[2:3]
	s_nop 0
	v_cvt_pk_bf16_f32 v36, v43, v45
	v_cvt_pk_bf16_f32 v37, v47, v49
	v_cvt_pk_bf16_f32 v38, v51, v95
	v_cvt_pk_bf16_f32 v39, v97, v101
	global_store_dwordx4 v[40:41], v[36:39], off
	s_waitcnt lgkmcnt(0)

; #pragma unroll 8
;     for (int i = 0; i < 32; ++i) { const int kk = 2 * i + (lane >> 5); scr[kk * 33 + (lane & 31)] = __builtin_nontemporal_load(W + (size_t)(k0 + kk) * ldw + n0 + (lane & 31)); }
; __device__ __forceinline__ void phase_p0a(const Ptrs& P, LAS unsigned char* lds, int tid_, int vcu, int G) {
;     ...
;             transpose_item(P.w_out + (size_t)l * 1024 * 1024, 1024, 64 * kb, 32 * nb, (bf16*)(P.ws + WS_WOUT) + ((size_t)l * 1024 + 32 * nb) * 1024 + 64 * kb, 1024, scr, lane); continue; }
.LBB0_67:
	v_lshl_add_u64 v[96:97], v[50:51], 0, s[42:43]
	s_waitcnt vmcnt(15)
	v_lshl_add_u64 v[98:99], v[48:49], 0, s[42:43]
	v_lshl_add_u64 v[100:101], v[46:47], 0, s[42:43]
	s_waitcnt vmcnt(14)
	v_lshl_add_u64 v[102:103], v[44:45], 0, s[42:43]
	v_lshl_add_u64 v[104:105], v[42:43], 0, s[42:43]
	s_waitcnt vmcnt(13)
	v_lshl_add_u64 v[106:107], v[40:41], 0, s[42:43]
	v_lshl_add_u64 v[108:109], v[38:39], 0, s[42:43]
	s_waitcnt vmcnt(12)
	v_lshl_add_u64 v[110:111], v[36:37], 0, s[42:43]
	global_load_dword v134, v[96:97], off nt
	s_nop 0
	global_load_dword v135, v[98:99], off nt
	s_nop 0
	global_load_dword v136, v[100:101], off nt
	global_load_dword v137, v[102:103], off nt
	s_nop 0
	global_load_dword v138, v[104:105], off nt
	global_load_dword v139, v[106:107], off nt
	global_load_dword v140, v[108:109], off nt
	global_load_dword v141, v[110:111], off nt
	s_add_u32 s42, s42, 0x10000
	s_addc_u32 s43, s43, 0
	v_lshl_add_u64 v[96:97], v[50:51], 0, s[42:43]
	v_lshl_add_u64 v[98:99], v[48:49], 0, s[42:43]
	v_lshl_add_u64 v[100:101], v[46:47], 0, s[42:43]
	v_lshl_add_u64 v[102:103], v[44:45], 0, s[42:43]
	v_lshl_add_u64 v[104:105], v[42:43], 0, s[42:43]
	v_lshl_add_u64 v[106:107], v[40:41], 0, s[42:43]
	v_lshl_add_u64 v[108:109], v[38:39], 0, s[42:43]
	v_lshl_add_u64 v[110:111], v[36:37], 0, s[42:43]
	global_load_dword v142, v[96:97], off nt
	s_nop 0
	global_load_dword v143, v[98:99], off nt
	s_nop 0
	global_load_dword v144, v[100:101], off nt
	global_load_dword v145, v[102:103], off nt
	s_nop 0
	global_load_dword v146, v[104:105], off nt
	global_load_dword v147, v[106:107], off nt
	global_load_dword v148, v[108:109], off nt
	global_load_dword v149, v[110:111], off nt
	s_add_u32 s42, s42, 0x10000
	s_addc_u32 s43, s43, 0
	v_lshl_add_u64 v[96:97], v[50:51], 0, s[42:43]
	v_lshl_add_u64 v[98:99], v[48:49], 0, s[42:43]
	v_lshl_add_u64 v[100:101], v[46:47], 0, s[42:43]
	v_lshl_add_u64 v[102:103], v[44:45], 0, s[42:43]
	v_lshl_add_u64 v[104:105], v[42:43], 0, s[42:43]
	v_lshl_add_u64 v[106:107], v[40:41], 0, s[42:43]
	v_lshl_add_u64 v[108:109], v[38:39], 0, s[42:43]
	v_lshl_add_u64 v[110:111], v[36:37], 0, s[42:43]
	global_load_dword v150, v[96:97], off nt
	s_nop 0
	global_load_dword v151, v[98:99], off nt
	s_nop 0
	global_load_dword v152, v[100:101], off nt
	global_load_dword v153, v[102:103], off nt
	s_nop 0
	global_load_dword v154, v[104:105], off nt
	global_load_dword v155, v[106:107], off nt
	global_load_dword v156, v[108:109], off nt
	global_load_dword v157, v[110:111], off nt
	s_add_u32 s42, s42, 0x10000
	s_addc_u32 s43, s43, 0
	v_lshl_add_u64 v[96:97], v[50:51], 0, s[42:43]
	v_lshl_add_u64 v[98:99], v[48:49], 0, s[42:43]
	v_lshl_add_u64 v[100:101], v[46:47], 0, s[42:43]
	v_lshl_add_u64 v[102:103], v[44:45], 0, s[42:43]
	v_lshl_add_u64 v[104:105], v[42:43], 0, s[42:43]
	v_lshl_add_u64 v[106:107], v[40:41], 0, s[42:43]
	v_lshl_add_u64 v[108:109], v[38:39], 0, s[42:43]
	v_lshl_add_u64 v[110:111], v[36:37], 0, s[42:43]
	global_load_dword v158, v[96:97], off nt
	s_nop 0
	global_load_dword v159, v[98:99], off nt
	s_nop 0
	global_load_dword v160, v[100:101], off nt
	global_load_dword v161, v[102:103], off nt
	s_nop 0
	global_load_dword v162, v[104:105], off nt
	global_load_dword v163, v[106:107], off nt
	global_load_dword v164, v[108:109], off nt
	global_load_dword v165, v[110:111], off nt
	s_add_u32 s42, s42, 0x10000
	s_addc_u32 s43, s43, 0
	v_add_u32_e32 v104, 0x400, v95
	s_waitcnt vmcnt(30)
	ds_write2_b32 v95, v134, v135 offset1:66
	s_waitcnt vmcnt(28)
	ds_write2_b32 v95, v136, v137 offset0:132 offset1:198
	s_waitcnt vmcnt(26)
	ds_write2_b32 v104, v138, v139 offset0:8 offset1:74
	s_waitcnt vmcnt(24)
; #define LAS __attribute__((address_space(3)))
; __device__ __forceinline__ unsigned pk2(float lo, float hi) { unsigned r; asm("v_cvt_pk_bf16_f32 %0, %1, %2" : "=v"(r) : "v"(lo), "v"(hi)); return r; }
; #define LDS_FENCE() asm volatile("s_waitcnt lgkmcnt(0)" ::: "memory")
;     ...
;     for (int i = 0; i < 32; ++i) { const int kk = 2 * i + (lane >> 5); scr[kk * 33 + (lane & 31)] = __builtin_nontemporal_load(W + (size_t)(k0 + kk) * ldw + n0 + (lane & 31)); }
;     LDS_FENCE();
;     const int c = lane & 7;
; #pragma unroll
;     for (int j = 0; j < 4; ++j) { const int n = (lane >> 3) + 8 * j; const LAS float* s = scr + (8 * c) * 33 + n;
;         v4u o; o.x = pk2(s[0 * 33], s[1 * 33]); o.y = pk2(s[2 * 33], s[3 * 33]); o.z = pk2(s[4 * 33], s[5 * 33]); o.w = pk2(s[6 * 33], s[7 * 33]);
;         int nr = n;
;         if (perm16) { const int cc = (n0 + n) & 255;
;             nr = (((cc >> 3) & 1) << 7) + ((cc >> 6) << 5) + (((cc >> 4) & 3) << 3) + (cc & 7) - (n0 & 255); }
;         if (fp8) {
;             v2u o8; o8.x = (unsigned)__builtin_amdgcn_cvt_pk_fp8_f32(s[2 * 33] * SW8, s[3 * 33] * SW8, __builtin_amdgcn_cvt_pk_fp8_f32(s[0 * 33] * SW8, s[1 * 33] * SW8, 0, false), true);
;             o8.y = (unsigned)__builtin_amdgcn_cvt_pk_fp8_f32(s[6 * 33] * SW8, s[7 * 33] * SW8, __builtin_amdgcn_cvt_pk_fp8_f32(s[4 * 33] * SW8, s[5 * 33] * SW8, 0, false), true);
;             *(v2u*)((unsigned char*)dst + (ptrdiff_t)nr * Kd + 8 * c) = o8;
;         } else *(v4u*)(dst + (ptrdiff_t)nr * Kd + 8 * c) = o; }
;     LDS_FENCE();
	ds_write2_b32 v104, v140, v141 offset0:140 offset1:206
	v_add_u32_e32 v95, 0x840, v95
	v_add_u32_e32 v104, 0x400, v95
	s_waitcnt vmcnt(22)
	ds_write2_b32 v95, v142, v143 offset1:66
	s_waitcnt vmcnt(20)
	ds_write2_b32 v95, v144, v145 offset0:132 offset1:198
	s_waitcnt vmcnt(18)
	ds_write2_b32 v104, v146, v147 offset0:8 offset1:74
	s_waitcnt vmcnt(16)
	ds_write2_b32 v104, v148, v149 offset0:140 offset1:206
	v_add_u32_e32 v95, 0x840, v95
	v_add_u32_e32 v104, 0x400, v95
	s_waitcnt vmcnt(14)
	ds_write2_b32 v95, v150, v151 offset1:66
	s_waitcnt vmcnt(12)
	ds_write2_b32 v95, v152, v153 offset0:132 offset1:198
	s_waitcnt vmcnt(10)
	ds_write2_b32 v104, v154, v155 offset0:8 offset1:74
	s_waitcnt vmcnt(8)
	ds_write2_b32 v104, v156, v157 offset0:140 offset1:206
	v_add_u32_e32 v95, 0x840, v95
	v_add_u32_e32 v104, 0x400, v95
	s_waitcnt vmcnt(6)
	ds_write2_b32 v95, v158, v159 offset1:66
	s_waitcnt vmcnt(4)
	ds_write2_b32 v95, v160, v161 offset0:132 offset1:198
	s_waitcnt vmcnt(2)
	ds_write2_b32 v104, v162, v163 offset0:8 offset1:74
	s_waitcnt vmcnt(0)
	ds_write2_b32 v104, v164, v165 offset0:140 offset1:206
	v_add_u32_e32 v95, 0x840, v95
	s_cmp_lg_u32 s42, 0x40000
	v_lshlrev_b64 v[38:39], 21, v[2:3]
	v_lshlrev_b32_e32 v2, 16, v35
	s_waitcnt lgkmcnt(0)
	v_add_u32_e32 v36, 0xfffff800, v94
	v_lshl_add_u64 v[38:39], s[12:13], 0, v[38:39]
	v_and_b32_e32 v2, 0x1f0000, v2
	ds_read2_b32 v[40:41], v7 offset0:33 offset1:41
	ds_read2_b32 v[42:43], v7 offset1:8
	ds_read2_b32 v[44:45], v7 offset0:66 offset1:74
	ds_read2_b32 v[46:47], v7 offset0:99 offset1:107
	ds_read2_b32 v[48:49], v7 offset0:132 offset1:140
	ds_read2_b32 v[50:51], v7 offset0:165 offset1:173
	ds_read2_b32 v[94:95], v7 offset0:198 offset1:206
	ds_read2_b32 v[96:97], v7 offset0:231 offset1:239
	v_mov_b32_e32 v37, v3
	v_lshl_add_u64 v[38:39], v[38:39], 0, v[2:3]
	v_lshl_add_u64 v[36:37], v[36:37], 1, v[38:39]
	v_lshlrev_b32_e32 v2, 1, v4
	v_lshl_add_u64 v[98:99], v[36:37], 0, v[2:3]
	v_lshlrev_b32_e32 v2, 1, v6
	v_lshl_add_u64 v[100:101], v[98:99], 0, v[2:3]
	s_waitcnt lgkmcnt(6)
	v_cvt_pk_bf16_f32 v36, v42, v40
	s_waitcnt lgkmcnt(4)
	v_cvt_pk_bf16_f32 v37, v44, v46
	s_waitcnt lgkmcnt(2)
	v_cvt_pk_bf16_f32 v38, v48, v50
	s_waitcnt lgkmcnt(0)
	v_cvt_pk_bf16_f32 v39, v94, v96
	global_store_dwordx4 v[100:101], v[36:39], off
	v_lshlrev_b32_e32 v2, 1, v8
	s_nop 0
	v_cvt_pk_bf16_f32 v36, v43, v41
	v_cvt_pk_bf16_f32 v37, v45, v47
	v_cvt_pk_bf16_f32 v38, v49, v51
	v_cvt_pk_bf16_f32 v39, v95, v97
	ds_read2_b32 v[42:43], v7 offset0:16 offset1:24
	ds_read2_b32 v[44:45], v7 offset0:49 offset1:57
	ds_read2_b32 v[46:47], v7 offset0:82 offset1:90
	ds_read2_b32 v[48:49], v7 offset0:115 offset1:123
	ds_read2_b32 v[50:51], v7 offset0:148 offset1:156
	ds_read2_b32 v[94:95], v7 offset0:181 offset1:189
	ds_read2_b32 v[96:97], v7 offset0:214 offset1:222
	ds_read2_b32 v[100:101], v7 offset0:247 offset1:255
	v_lshl_add_u64 v[40:41], v[98:99], 0, v[2:3]
	v_lshlrev_b32_e32 v2, 1, v10
	global_store_dwordx4 v[40:41], v[36:39], off
	v_lshl_add_u64 v[40:41], v[98:99], 0, v[2:3]
	v_lshlrev_b32_e32 v2, 1, v12
	s_waitcnt lgkmcnt(6)
	v_cvt_pk_bf16_f32 v36, v42, v44
	s_waitcnt lgkmcnt(4)
	v_cvt_pk_bf16_f32 v37, v46, v48
	s_waitcnt lgkmcnt(2)
	v_cvt_pk_bf16_f32 v38, v50, v94
	s_waitcnt lgkmcnt(0)
	v_cvt_pk_bf16_f32 v39, v96, v100
	global_store_dwordx4 v[40:41], v[36:39], off
	v_lshl_add_u64 v[40:41], v[98:99], 0, v[2:3]
	s_nop 0
	v_cvt_pk_bf16_f32 v36, v43, v45
	v_cvt_pk_bf16_f32 v37, v47, v49
	v_cvt_pk_bf16_f32 v38, v51, v95
	v_cvt_pk_bf16_f32 v39, v97, v101
	global_store_dwordx4 v[40:41], v[36:39], off
	s_waitcnt lgkmcnt(0)

; #pragma unroll 8
;     for (int i = 0; i < 32; ++i) { const int kk = 2 * i + (lane >> 5); scr[kk * 33 + (lane & 31)] = __builtin_nontemporal_load(W + (size_t)(k0 + kk) * ldw + n0 + (lane & 31)); }
; __device__ __forceinline__ void phase_p0a(const Ptrs& P, LAS unsigned char* lds, int tid_, int vcu, int G) {
;     ...
;             transpose_item(P.w_in + (size_t)l * 1024 * DIN, DIN, 64 * kb, 256 + 32 * nb, (bf16*)(P.ws + WS_WIN) + ((size_t)l * 2048 + 32 * nb) * 1024 + 64 * kb, 1024, scr, lane); continue; }
.LBB0_72:
	v_add_u32_e32 v41, s36, v35
	v_add_u32_e32 v44, 2, v41
	v_add_u32_e32 v46, 4, v41
	v_add_u32_e32 v48, 6, v41
	v_mad_i64_i32 v[42:43], s[42:43], v41, s61, v[38:39]
	v_add_u32_e32 v50, 8, v41
	s_waitcnt vmcnt(16)
	v_add_u32_e32 v94, 10, v41
	v_add_u32_e32 v96, 12, v41
	v_add_u32_e32 v41, 14, v41
	v_mad_i64_i32 v[44:45], s[42:43], v44, s61, v[38:39]
	v_mad_i64_i32 v[46:47], s[42:43], v46, s61, v[38:39]
	v_mad_i64_i32 v[48:49], s[42:43], v48, s61, v[38:39]
	v_mad_i64_i32 v[50:51], s[42:43], v50, s61, v[38:39]
	v_mad_i64_i32 v[94:95], s[42:43], v94, s61, v[38:39]
	v_mad_i64_i32 v[96:97], s[42:43], v96, s61, v[38:39]
	s_waitcnt vmcnt(15)
	v_mad_i64_i32 v[98:99], s[42:43], v41, s61, v[38:39]
	global_load_dword v134, v[42:43], off offset:1024 nt
	s_nop 0
	global_load_dword v135, v[44:45], off offset:1024 nt
	global_load_dword v136, v[46:47], off offset:1024 nt
	s_nop 0
	global_load_dword v137, v[48:49], off offset:1024 nt
	global_load_dword v138, v[50:51], off offset:1024 nt
	global_load_dword v139, v[94:95], off offset:1024 nt
	global_load_dword v140, v[96:97], off offset:1024 nt
	s_nop 0
	global_load_dword v141, v[98:99], off offset:1024 nt
	s_add_i32 s36, s36, 16
	v_add_u32_e32 v41, s36, v35
	v_add_u32_e32 v44, 2, v41
	v_add_u32_e32 v46, 4, v41
	v_add_u32_e32 v48, 6, v41
	v_mad_i64_i32 v[42:43], s[42:43], v41, s61, v[38:39]
	v_add_u32_e32 v50, 8, v41
	v_add_u32_e32 v94, 10, v41
	v_add_u32_e32 v96, 12, v41
	v_add_u32_e32 v41, 14, v41
	v_mad_i64_i32 v[44:45], s[42:43], v44, s61, v[38:39]
	v_mad_i64_i32 v[46:47], s[42:43], v46, s61, v[38:39]
	v_mad_i64_i32 v[48:49], s[42:43], v48, s61, v[38:39]
	v_mad_i64_i32 v[50:51], s[42:43], v50, s61, v[38:39]
	v_mad_i64_i32 v[94:95], s[42:43], v94, s61, v[38:39]
	v_mad_i64_i32 v[96:97], s[42:43], v96, s61, v[38:39]
	v_mad_i64_i32 v[98:99], s[42:43], v41, s61, v[38:39]
	global_load_dword v142, v[42:43], off offset:1024 nt
	s_nop 0
	global_load_dword v143, v[44:45], off offset:1024 nt
	global_load_dword v144, v[46:47], off offset:1024 nt
	s_nop 0
	global_load_dword v145, v[48:49], off offset:1024 nt
	global_load_dword v146, v[50:51], off offset:1024 nt
	global_load_dword v147, v[94:95], off offset:1024 nt
	global_load_dword v148, v[96:97], off offset:1024 nt
	s_nop 0
	global_load_dword v149, v[98:99], off offset:1024 nt
	s_add_i32 s36, s36, 16
	v_add_u32_e32 v41, s36, v35
	v_add_u32_e32 v44, 2, v41
	v_add_u32_e32 v46, 4, v41
	v_add_u32_e32 v48, 6, v41
	v_mad_i64_i32 v[42:43], s[42:43], v41, s61, v[38:39]
	v_add_u32_e32 v50, 8, v41
	v_add_u32_e32 v94, 10, v41
	v_add_u32_e32 v96, 12, v41
	v_add_u32_e32 v41, 14, v41
	v_mad_i64_i32 v[44:45], s[42:43], v44, s61, v[38:39]
	v_mad_i64_i32 v[46:47], s[42:43], v46, s61, v[38:39]
	v_mad_i64_i32 v[48:49], s[42:43], v48, s61, v[38:39]
	v_mad_i64_i32 v[50:51], s[42:43], v50, s61, v[38:39]
	v_mad_i64_i32 v[94:95], s[42:43], v94, s61, v[38:39]
	v_mad_i64_i32 v[96:97], s[42:43], v96, s61, v[38:39]
	v_mad_i64_i32 v[98:99], s[42:43], v41, s61, v[38:39]
	global_load_dword v150, v[42:43], off offset:1024 nt
	s_nop 0
	global_load_dword v151, v[44:45], off offset:1024 nt
	global_load_dword v152, v[46:47], off offset:1024 nt
	s_nop 0
	global_load_dword v153, v[48:49], off offset:1024 nt
	global_load_dword v154, v[50:51], off offset:1024 nt
	global_load_dword v155, v[94:95], off offset:1024 nt
	global_load_dword v156, v[96:97], off offset:1024 nt
	s_nop 0
	global_load_dword v157, v[98:99], off offset:1024 nt
	s_add_i32 s36, s36, 16
	v_add_u32_e32 v41, s36, v35
	v_add_u32_e32 v44, 2, v41
	v_add_u32_e32 v46, 4, v41
	v_add_u32_e32 v48, 6, v41
	v_mad_i64_i32 v[42:43], s[42:43], v41, s61, v[38:39]
	v_add_u32_e32 v50, 8, v41
	v_add_u32_e32 v94, 10, v41
	v_add_u32_e32 v96, 12, v41
	v_add_u32_e32 v41, 14, v41
	v_mad_i64_i32 v[44:45], s[42:43], v44, s61, v[38:39]
	v_mad_i64_i32 v[46:47], s[42:43], v46, s61, v[38:39]
	v_mad_i64_i32 v[48:49], s[42:43], v48, s61, v[38:39]
	v_mad_i64_i32 v[50:51], s[42:43], v50, s61, v[38:39]
	v_mad_i64_i32 v[94:95], s[42:43], v94, s61, v[38:39]
	v_mad_i64_i32 v[96:97], s[42:43], v96, s61, v[38:39]
	v_mad_i64_i32 v[98:99], s[42:43], v41, s61, v[38:39]
	global_load_dword v158, v[42:43], off offset:1024 nt
	s_nop 0
	global_load_dword v159, v[44:45], off offset:1024 nt
	global_load_dword v160, v[46:47], off offset:1024 nt
	s_nop 0
	global_load_dword v161, v[48:49], off offset:1024 nt
	global_load_dword v162, v[50:51], off offset:1024 nt
	global_load_dword v163, v[94:95], off offset:1024 nt
	global_load_dword v164, v[96:97], off offset:1024 nt
	s_nop 0
	global_load_dword v165, v[98:99], off offset:1024 nt
	s_add_i32 s36, s36, 16
	v_add_u32_e32 v49, 0x400, v37
	s_waitcnt vmcnt(30)
; #define LAS __attribute__((address_space(3)))
; __device__ __forceinline__ unsigned pk2(float lo, float hi) { unsigned r; asm("v_cvt_pk_bf16_f32 %0, %1, %2" : "=v"(r) : "v"(lo), "v"(hi)); return r; }
; #define LDS_FENCE() asm volatile("s_waitcnt lgkmcnt(0)" ::: "memory")
;     ...
;     for (int i = 0; i < 32; ++i) { const int kk = 2 * i + (lane >> 5); scr[kk * 33 + (lane & 31)] = __builtin_nontemporal_load(W + (size_t)(k0 + kk) * ldw + n0 + (lane & 31)); }
;     LDS_FENCE();
;     const int c = lane & 7;
; #pragma unroll
;     for (int j = 0; j < 4; ++j) { const int n = (lane >> 3) + 8 * j; const LAS float* s = scr + (8 * c) * 33 + n;
;         v4u o; o.x = pk2(s[0 * 33], s[1 * 33]); o.y = pk2(s[2 * 33], s[3 * 33]); o.z = pk2(s[4 * 33], s[5 * 33]); o.w = pk2(s[6 * 33], s[7 * 33]);
;         int nr = n;
;         if (perm16) { const int cc = (n0 + n) & 255;
;             nr = (((cc >> 3) & 1) << 7) + ((cc >> 6) << 5) + (((cc >> 4) & 3) << 3) + (cc & 7) - (n0 & 255); }
;         if (fp8) {
;             v2u o8; o8.x = (unsigned)__builtin_amdgcn_cvt_pk_fp8_f32(s[2 * 33] * SW8, s[3 * 33] * SW8, __builtin_amdgcn_cvt_pk_fp8_f32(s[0 * 33] * SW8, s[1 * 33] * SW8, 0, false), true);
;             o8.y = (unsigned)__builtin_amdgcn_cvt_pk_fp8_f32(s[6 * 33] * SW8, s[7 * 33] * SW8, __builtin_amdgcn_cvt_pk_fp8_f32(s[4 * 33] * SW8, s[5 * 33] * SW8, 0, false), true);
;             *(v2u*)((unsigned char*)dst + (ptrdiff_t)nr * Kd + 8 * c) = o8;
;         } else *(v4u*)(dst + (ptrdiff_t)nr * Kd + 8 * c) = o; }
;     LDS_FENCE();
	ds_write2_b32 v37, v134, v135 offset1:66
	s_waitcnt vmcnt(28)
	ds_write2_b32 v37, v136, v137 offset0:132 offset1:198
	s_waitcnt vmcnt(26)
	ds_write2_b32 v49, v138, v139 offset0:8 offset1:74
	s_waitcnt vmcnt(24)
	ds_write2_b32 v49, v140, v141 offset0:140 offset1:206
	v_add_u32_e32 v37, 0x840, v37
	v_add_u32_e32 v49, 0x400, v37
	s_waitcnt vmcnt(22)
	ds_write2_b32 v37, v142, v143 offset1:66
	s_waitcnt vmcnt(20)
	ds_write2_b32 v37, v144, v145 offset0:132 offset1:198
	s_waitcnt vmcnt(18)
	ds_write2_b32 v49, v146, v147 offset0:8 offset1:74
	s_waitcnt vmcnt(16)
	ds_write2_b32 v49, v148, v149 offset0:140 offset1:206
	v_add_u32_e32 v37, 0x840, v37
	v_add_u32_e32 v49, 0x400, v37
	s_waitcnt vmcnt(14)
	ds_write2_b32 v37, v150, v151 offset1:66
	s_waitcnt vmcnt(12)
	ds_write2_b32 v37, v152, v153 offset0:132 offset1:198
	s_waitcnt vmcnt(10)
	ds_write2_b32 v49, v154, v155 offset0:8 offset1:74
	s_waitcnt vmcnt(8)
	ds_write2_b32 v49, v156, v157 offset0:140 offset1:206
	v_add_u32_e32 v37, 0x840, v37
	v_add_u32_e32 v49, 0x400, v37
	s_waitcnt vmcnt(6)
	ds_write2_b32 v37, v158, v159 offset1:66
	s_waitcnt vmcnt(4)
	ds_write2_b32 v37, v160, v161 offset0:132 offset1:198
	s_waitcnt vmcnt(2)
	ds_write2_b32 v49, v162, v163 offset0:8 offset1:74
	s_waitcnt vmcnt(0)
	ds_write2_b32 v49, v164, v165 offset0:140 offset1:206
	v_add_u32_e32 v37, 0x840, v37
	s_cmp_lg_u32 s36, 64
	v_lshlrev_b64 v[38:39], 22, v[2:3]
	s_waitcnt lgkmcnt(0)
	v_lshl_add_u64 v[38:39], s[38:39], 0, v[38:39]
	v_lshlrev_b32_e32 v2, 11, v40
	ds_read2_b32 v[40:41], v7 offset0:33 offset1:41
	ds_read2_b32 v[42:43], v7 offset1:8
	ds_read2_b32 v[44:45], v7 offset0:66 offset1:74
	ds_read2_b32 v[46:47], v7 offset0:99 offset1:107
	ds_read2_b32 v[48:49], v7 offset0:132 offset1:140
	ds_read2_b32 v[50:51], v7 offset0:165 offset1:173
	ds_read2_b32 v[94:95], v7 offset0:198 offset1:206
	ds_read2_b32 v[96:97], v7 offset0:231 offset1:239
	v_ashrrev_i32_e32 v37, 31, v36
	v_lshl_add_u64 v[38:39], v[38:39], 0, v[2:3]
	v_lshl_add_u64 v[36:37], v[36:37], 1, v[38:39]
	v_lshlrev_b32_e32 v2, 1, v4
	v_lshl_add_u64 v[98:99], v[36:37], 0, v[2:3]
	v_lshlrev_b32_e32 v2, 1, v6
	v_lshl_add_u64 v[100:101], v[98:99], 0, v[2:3]
	s_waitcnt lgkmcnt(6)
	v_cvt_pk_bf16_f32 v36, v42, v40
	s_waitcnt lgkmcnt(4)
	v_cvt_pk_bf16_f32 v37, v44, v46
	s_waitcnt lgkmcnt(2)
	v_cvt_pk_bf16_f32 v38, v48, v50
	s_waitcnt lgkmcnt(0)
	v_cvt_pk_bf16_f32 v39, v94, v96
	global_store_dwordx4 v[100:101], v[36:39], off
	v_lshlrev_b32_e32 v2, 1, v8
	s_nop 0
	v_cvt_pk_bf16_f32 v36, v43, v41
	v_cvt_pk_bf16_f32 v37, v45, v47
	v_cvt_pk_bf16_f32 v38, v49, v51
	v_cvt_pk_bf16_f32 v39, v95, v97
	ds_read2_b32 v[42:43], v7 offset0:16 offset1:24
	ds_read2_b32 v[44:45], v7 offset0:49 offset1:57
	ds_read2_b32 v[46:47], v7 offset0:82 offset1:90
	ds_read2_b32 v[48:49], v7 offset0:115 offset1:123
	ds_read2_b32 v[50:51], v7 offset0:148 offset1:156
	ds_read2_b32 v[94:95], v7 offset0:181 offset1:189
	ds_read2_b32 v[96:97], v7 offset0:214 offset1:222
	ds_read2_b32 v[100:101], v7 offset0:247 offset1:255
	v_lshl_add_u64 v[40:41], v[98:99], 0, v[2:3]
	v_lshlrev_b32_e32 v2, 1, v10
	global_store_dwordx4 v[40:41], v[36:39], off
	v_lshl_add_u64 v[40:41], v[98:99], 0, v[2:3]
	v_lshlrev_b32_e32 v2, 1, v12
	s_waitcnt lgkmcnt(6)
	v_cvt_pk_bf16_f32 v36, v42, v44
	s_waitcnt lgkmcnt(4)
	v_cvt_pk_bf16_f32 v37, v46, v48
	s_waitcnt lgkmcnt(2)
	v_cvt_pk_bf16_f32 v38, v50, v94
	s_waitcnt lgkmcnt(0)
	v_cvt_pk_bf16_f32 v39, v96, v100
	global_store_dwordx4 v[40:41], v[36:39], off
	v_lshl_add_u64 v[40:41], v[98:99], 0, v[2:3]
	s_nop 0
	v_cvt_pk_bf16_f32 v36, v43, v45
	v_cvt_pk_bf16_f32 v37, v47, v49
	v_cvt_pk_bf16_f32 v38, v51, v95
	v_cvt_pk_bf16_f32 v39, v97, v101
	global_store_dwordx4 v[40:41], v[36:39], off
	s_waitcnt lgkmcnt(0)

; #pragma unroll 8
;     for (int i = 0; i < 32; ++i) { const int kk = 2 * i + (lane >> 5); scr[kk * 33 + (lane & 31)] = __builtin_nontemporal_load(W + (size_t)(k0 + kk) * ldw + n0 + (lane & 31)); }
; __device__ __forceinline__ void phase_p0a(const Ptrs& P, LAS unsigned char* lds, int tid_, int vcu, int G) {
;     ...
;                 else { bf16* dst = (bf16*)(P.ws + WS_WD + (size_t)l * WD_L) + (size_t)n0 * 256 + k0; transpose_item(sd, 1024, k0, n0, dst, 256, scr, lane, 0); } }
.LBB0_78:
	v_lshl_add_u64 v[96:97], v[36:37], 0, s[36:37]
	v_lshl_add_u64 v[98:99], v[50:51], 0, s[36:37]
	v_lshl_add_u64 v[100:101], v[48:49], 0, s[36:37]
	s_waitcnt vmcnt(14)
	v_lshl_add_u64 v[102:103], v[46:47], 0, s[36:37]
	v_lshl_add_u64 v[104:105], v[44:45], 0, s[36:37]
	s_waitcnt vmcnt(13)
	v_lshl_add_u64 v[106:107], v[42:43], 0, s[36:37]
	v_lshl_add_u64 v[108:109], v[40:41], 0, s[36:37]
	s_waitcnt vmcnt(12)
	v_lshl_add_u64 v[110:111], v[38:39], 0, s[36:37]
	global_load_dword v134, v[96:97], off nt
	s_nop 0
	global_load_dword v135, v[98:99], off nt
	s_nop 0
	global_load_dword v136, v[100:101], off nt
	global_load_dword v137, v[102:103], off nt
	s_nop 0
	global_load_dword v138, v[104:105], off nt
	global_load_dword v139, v[106:107], off nt
	global_load_dword v140, v[108:109], off nt
	global_load_dword v141, v[110:111], off nt
	s_add_u32 s36, s36, 0x10000
	s_addc_u32 s37, s37, 0
	v_lshl_add_u64 v[96:97], v[36:37], 0, s[36:37]
	v_lshl_add_u64 v[98:99], v[50:51], 0, s[36:37]
	v_lshl_add_u64 v[100:101], v[48:49], 0, s[36:37]
	v_lshl_add_u64 v[102:103], v[46:47], 0, s[36:37]
	v_lshl_add_u64 v[104:105], v[44:45], 0, s[36:37]
	v_lshl_add_u64 v[106:107], v[42:43], 0, s[36:37]
	v_lshl_add_u64 v[108:109], v[40:41], 0, s[36:37]
	v_lshl_add_u64 v[110:111], v[38:39], 0, s[36:37]
	global_load_dword v142, v[96:97], off nt
	s_nop 0
	global_load_dword v143, v[98:99], off nt
	s_nop 0
	global_load_dword v144, v[100:101], off nt
	global_load_dword v145, v[102:103], off nt
	s_nop 0
	global_load_dword v146, v[104:105], off nt
	global_load_dword v147, v[106:107], off nt
	global_load_dword v148, v[108:109], off nt
	global_load_dword v149, v[110:111], off nt
	s_add_u32 s36, s36, 0x10000
	s_addc_u32 s37, s37, 0
	v_lshl_add_u64 v[96:97], v[36:37], 0, s[36:37]
	v_lshl_add_u64 v[98:99], v[50:51], 0, s[36:37]
	v_lshl_add_u64 v[100:101], v[48:49], 0, s[36:37]
	v_lshl_add_u64 v[102:103], v[46:47], 0, s[36:37]
	v_lshl_add_u64 v[104:105], v[44:45], 0, s[36:37]
	v_lshl_add_u64 v[106:107], v[42:43], 0, s[36:37]
	v_lshl_add_u64 v[108:109], v[40:41], 0, s[36:37]
	v_lshl_add_u64 v[110:111], v[38:39], 0, s[36:37]
	global_load_dword v150, v[96:97], off nt
	s_nop 0
	global_load_dword v151, v[98:99], off nt
	s_nop 0
	global_load_dword v152, v[100:101], off nt
	global_load_dword v153, v[102:103], off nt
	s_nop 0
	global_load_dword v154, v[104:105], off nt
	global_load_dword v155, v[106:107], off nt
	global_load_dword v156, v[108:109], off nt
	global_load_dword v157, v[110:111], off nt
	s_add_u32 s36, s36, 0x10000
	s_addc_u32 s37, s37, 0
	v_lshl_add_u64 v[96:97], v[36:37], 0, s[36:37]
	v_lshl_add_u64 v[98:99], v[50:51], 0, s[36:37]
	v_lshl_add_u64 v[100:101], v[48:49], 0, s[36:37]
	v_lshl_add_u64 v[102:103], v[46:47], 0, s[36:37]
	v_lshl_add_u64 v[104:105], v[44:45], 0, s[36:37]
	v_lshl_add_u64 v[106:107], v[42:43], 0, s[36:37]
	v_lshl_add_u64 v[108:109], v[40:41], 0, s[36:37]
	v_lshl_add_u64 v[110:111], v[38:39], 0, s[36:37]
	global_load_dword v158, v[96:97], off nt
	s_nop 0
	global_load_dword v159, v[98:99], off nt
	s_nop 0
	global_load_dword v160, v[100:101], off nt
	global_load_dword v161, v[102:103], off nt
	s_nop 0
	global_load_dword v162, v[104:105], off nt
	global_load_dword v163, v[106:107], off nt
	global_load_dword v164, v[108:109], off nt
	global_load_dword v165, v[110:111], off nt
	s_add_u32 s36, s36, 0x10000
	s_addc_u32 s37, s37, 0
	v_add_u32_e32 v104, 0x400, v35
	s_waitcnt vmcnt(30)
	ds_write2_b32 v35, v134, v135 offset1:66
	s_waitcnt vmcnt(28)
	ds_write2_b32 v35, v136, v137 offset0:132 offset1:198
	s_waitcnt vmcnt(26)
	ds_write2_b32 v104, v138, v139 offset0:8 offset1:74
	s_waitcnt vmcnt(24)
; #define LAS __attribute__((address_space(3)))
; __device__ __forceinline__ unsigned pk2(float lo, float hi) { unsigned r; asm("v_cvt_pk_bf16_f32 %0, %1, %2" : "=v"(r) : "v"(lo), "v"(hi)); return r; }
; #define LDS_FENCE() asm volatile("s_waitcnt lgkmcnt(0)" ::: "memory")
;     ...
;     for (int i = 0; i < 32; ++i) { const int kk = 2 * i + (lane >> 5); scr[kk * 33 + (lane & 31)] = __builtin_nontemporal_load(W + (size_t)(k0 + kk) * ldw + n0 + (lane & 31)); }
;     LDS_FENCE();
;     const int c = lane & 7;
; #pragma unroll
;     for (int j = 0; j < 4; ++j) { const int n = (lane >> 3) + 8 * j; const LAS float* s = scr + (8 * c) * 33 + n;
;         v4u o; o.x = pk2(s[0 * 33], s[1 * 33]); o.y = pk2(s[2 * 33], s[3 * 33]); o.z = pk2(s[4 * 33], s[5 * 33]); o.w = pk2(s[6 * 33], s[7 * 33]);
;         int nr = n;
;         if (perm16) { const int cc = (n0 + n) & 255;
;             nr = (((cc >> 3) & 1) << 7) + ((cc >> 6) << 5) + (((cc >> 4) & 3) << 3) + (cc & 7) - (n0 & 255); }
;         if (fp8) {
;             v2u o8; o8.x = (unsigned)__builtin_amdgcn_cvt_pk_fp8_f32(s[2 * 33] * SW8, s[3 * 33] * SW8, __builtin_amdgcn_cvt_pk_fp8_f32(s[0 * 33] * SW8, s[1 * 33] * SW8, 0, false), true);
;             o8.y = (unsigned)__builtin_amdgcn_cvt_pk_fp8_f32(s[6 * 33] * SW8, s[7 * 33] * SW8, __builtin_amdgcn_cvt_pk_fp8_f32(s[4 * 33] * SW8, s[5 * 33] * SW8, 0, false), true);
;             *(v2u*)((unsigned char*)dst + (ptrdiff_t)nr * Kd + 8 * c) = o8;
;         } else *(v4u*)(dst + (ptrdiff_t)nr * Kd + 8 * c) = o; }
;     LDS_FENCE();
	ds_write2_b32 v104, v140, v141 offset0:140 offset1:206
	v_add_u32_e32 v35, 0x840, v35
	v_add_u32_e32 v104, 0x400, v35
	s_waitcnt vmcnt(22)
	ds_write2_b32 v35, v142, v143 offset1:66
	s_waitcnt vmcnt(20)
	ds_write2_b32 v35, v144, v145 offset0:132 offset1:198
	s_waitcnt vmcnt(18)
	ds_write2_b32 v104, v146, v147 offset0:8 offset1:74
	s_waitcnt vmcnt(16)
	ds_write2_b32 v104, v148, v149 offset0:140 offset1:206
	v_add_u32_e32 v35, 0x840, v35
	v_add_u32_e32 v104, 0x400, v35
	s_waitcnt vmcnt(14)
	ds_write2_b32 v35, v150, v151 offset1:66
	s_waitcnt vmcnt(12)
	ds_write2_b32 v35, v152, v153 offset0:132 offset1:198
	s_waitcnt vmcnt(10)
	ds_write2_b32 v104, v154, v155 offset0:8 offset1:74
	s_waitcnt vmcnt(8)
	ds_write2_b32 v104, v156, v157 offset0:140 offset1:206
	v_add_u32_e32 v35, 0x840, v35
	v_add_u32_e32 v104, 0x400, v35
	s_waitcnt vmcnt(6)
	ds_write2_b32 v35, v158, v159 offset1:66
	s_waitcnt vmcnt(4)
	ds_write2_b32 v35, v160, v161 offset0:132 offset1:198
	s_waitcnt vmcnt(2)
	ds_write2_b32 v104, v162, v163 offset0:8 offset1:74
	s_waitcnt vmcnt(0)
	ds_write2_b32 v104, v164, v165 offset0:140 offset1:206
	v_add_u32_e32 v35, 0x840, v35
	s_cmp_lg_u32 s36, 0x40000
	v_and_b32_e32 v35, 0x3e0, v94
	v_mov_b64_e32 v[38:39], s[40:41]
	s_waitcnt lgkmcnt(0)
	v_add_u32_e32 v36, 0xffffec80, v95
	v_mad_u64_u32 v[38:39], s[36:37], v2, s63, v[38:39]
	v_lshlrev_b32_e32 v2, 9, v35
	ds_read2_b32 v[40:41], v7 offset0:33 offset1:41
	ds_read2_b32 v[42:43], v7 offset1:8
	ds_read2_b32 v[44:45], v7 offset0:66 offset1:74
	ds_read2_b32 v[46:47], v7 offset0:99 offset1:107
	ds_read2_b32 v[48:49], v7 offset0:132 offset1:140
	ds_read2_b32 v[50:51], v7 offset0:165 offset1:173
	ds_read2_b32 v[94:95], v7 offset0:198 offset1:206
	ds_read2_b32 v[96:97], v7 offset0:231 offset1:239
	v_mov_b32_e32 v37, v3
	v_lshl_add_u64 v[38:39], v[38:39], 0, v[2:3]
	v_lshl_add_u64 v[36:37], v[36:37], 1, v[38:39]
	v_lshlrev_b32_e32 v2, 1, v4
	v_lshl_add_u64 v[98:99], v[36:37], 0, v[2:3]
	v_lshlrev_b32_e32 v2, 1, v14
	v_lshl_add_u64 v[100:101], v[98:99], 0, v[2:3]
	s_waitcnt lgkmcnt(6)
	v_cvt_pk_bf16_f32 v36, v42, v40
	s_waitcnt lgkmcnt(4)
	v_cvt_pk_bf16_f32 v37, v44, v46
	s_waitcnt lgkmcnt(2)
	v_cvt_pk_bf16_f32 v38, v48, v50
	s_waitcnt lgkmcnt(0)
	v_cvt_pk_bf16_f32 v39, v94, v96
	global_store_dwordx4 v[100:101], v[36:39], off
	v_lshlrev_b32_e32 v2, 1, v16
	s_nop 0
	v_cvt_pk_bf16_f32 v36, v43, v41
	v_cvt_pk_bf16_f32 v37, v45, v47
	v_cvt_pk_bf16_f32 v38, v49, v51
	v_cvt_pk_bf16_f32 v39, v95, v97
	ds_read2_b32 v[42:43], v7 offset0:16 offset1:24
	ds_read2_b32 v[44:45], v7 offset0:49 offset1:57
	ds_read2_b32 v[46:47], v7 offset0:82 offset1:90
	ds_read2_b32 v[48:49], v7 offset0:115 offset1:123
	ds_read2_b32 v[50:51], v7 offset0:148 offset1:156
	ds_read2_b32 v[94:95], v7 offset0:181 offset1:189
	ds_read2_b32 v[96:97], v7 offset0:214 offset1:222
	ds_read2_b32 v[100:101], v7 offset0:247 offset1:255
	v_lshl_add_u64 v[40:41], v[98:99], 0, v[2:3]
	v_lshlrev_b32_e32 v2, 1, v18
	global_store_dwordx4 v[40:41], v[36:39], off
	v_lshl_add_u64 v[40:41], v[98:99], 0, v[2:3]
	v_lshlrev_b32_e32 v2, 1, v20
	s_waitcnt lgkmcnt(6)
	v_cvt_pk_bf16_f32 v36, v42, v44
	s_waitcnt lgkmcnt(4)
	v_cvt_pk_bf16_f32 v37, v46, v48
	s_waitcnt lgkmcnt(2)
	v_cvt_pk_bf16_f32 v38, v50, v94
	s_waitcnt lgkmcnt(0)
	v_cvt_pk_bf16_f32 v39, v96, v100
	global_store_dwordx4 v[40:41], v[36:39], off
	v_lshl_add_u64 v[40:41], v[98:99], 0, v[2:3]
	s_nop 0
	v_cvt_pk_bf16_f32 v36, v43, v45
	v_cvt_pk_bf16_f32 v37, v47, v49
	v_cvt_pk_bf16_f32 v38, v51, v95
	v_cvt_pk_bf16_f32 v39, v97, v101
	global_store_dwordx4 v[40:41], v[36:39], off
	s_waitcnt lgkmcnt(0)

; #pragma unroll 8
;     for (int i = 0; i < 32; ++i) { const int kk = 2 * i + (lane >> 5); scr[kk * 33 + (lane & 31)] = __builtin_nontemporal_load(W + (size_t)(k0 + kk) * ldw + n0 + (lane & 31)); }
; __device__ __forceinline__ void phase_p0a(const Ptrs& P, LAS unsigned char* lds, int tid_, int vcu, int G) {
;     ...
;                     transpose_item(up ? su : sg, 256, k0, n0, dst, 1024, scr, lane); } }
.LBB0_82:
	v_lshl_add_u64 v[98:99], v[50:51], 0, s[36:37]
	v_lshl_add_u64 v[100:101], v[48:49], 0, s[36:37]
	s_waitcnt vmcnt(14)
	v_lshl_add_u64 v[102:103], v[46:47], 0, s[36:37]
	v_lshl_add_u64 v[104:105], v[44:45], 0, s[36:37]
	s_waitcnt vmcnt(13)
	v_lshl_add_u64 v[106:107], v[42:43], 0, s[36:37]
	v_lshl_add_u64 v[108:109], v[40:41], 0, s[36:37]
	s_waitcnt vmcnt(12)
	v_lshl_add_u64 v[110:111], v[38:39], 0, s[36:37]
	v_lshl_add_u64 v[112:113], v[36:37], 0, s[36:37]
	global_load_dword v134, v[98:99], off nt
	s_nop 0
	global_load_dword v135, v[100:101], off nt
	global_load_dword v136, v[102:103], off nt
	s_nop 0
	global_load_dword v137, v[104:105], off nt
	global_load_dword v138, v[106:107], off nt
	global_load_dword v139, v[108:109], off nt
	global_load_dword v140, v[110:111], off nt
	s_nop 0
	global_load_dword v141, v[112:113], off nt
	s_add_u32 s36, s36, 0x4000
	s_addc_u32 s37, s37, 0
	v_lshl_add_u64 v[98:99], v[50:51], 0, s[36:37]
	v_lshl_add_u64 v[100:101], v[48:49], 0, s[36:37]
	v_lshl_add_u64 v[102:103], v[46:47], 0, s[36:37]
	v_lshl_add_u64 v[104:105], v[44:45], 0, s[36:37]
	v_lshl_add_u64 v[106:107], v[42:43], 0, s[36:37]
	v_lshl_add_u64 v[108:109], v[40:41], 0, s[36:37]
	v_lshl_add_u64 v[110:111], v[38:39], 0, s[36:37]
	v_lshl_add_u64 v[112:113], v[36:37], 0, s[36:37]
	global_load_dword v142, v[98:99], off nt
	s_nop 0
	global_load_dword v143, v[100:101], off nt
	global_load_dword v144, v[102:103], off nt
	s_nop 0
	global_load_dword v145, v[104:105], off nt
	global_load_dword v146, v[106:107], off nt
	global_load_dword v147, v[108:109], off nt
	global_load_dword v148, v[110:111], off nt
	s_nop 0
	global_load_dword v149, v[112:113], off nt
	s_add_u32 s36, s36, 0x4000
	s_addc_u32 s37, s37, 0
	v_lshl_add_u64 v[98:99], v[50:51], 0, s[36:37]
	v_lshl_add_u64 v[100:101], v[48:49], 0, s[36:37]
	v_lshl_add_u64 v[102:103], v[46:47], 0, s[36:37]
	v_lshl_add_u64 v[104:105], v[44:45], 0, s[36:37]
	v_lshl_add_u64 v[106:107], v[42:43], 0, s[36:37]
	v_lshl_add_u64 v[108:109], v[40:41], 0, s[36:37]
	v_lshl_add_u64 v[110:111], v[38:39], 0, s[36:37]
	v_lshl_add_u64 v[112:113], v[36:37], 0, s[36:37]
	global_load_dword v150, v[98:99], off nt
	s_nop 0
	global_load_dword v151, v[100:101], off nt
	global_load_dword v152, v[102:103], off nt
	s_nop 0
	global_load_dword v153, v[104:105], off nt
	global_load_dword v154, v[106:107], off nt
	global_load_dword v155, v[108:109], off nt
	global_load_dword v156, v[110:111], off nt
	s_nop 0
	global_load_dword v157, v[112:113], off nt
	s_add_u32 s36, s36, 0x4000
	s_addc_u32 s37, s37, 0
	v_lshl_add_u64 v[98:99], v[50:51], 0, s[36:37]
	v_lshl_add_u64 v[100:101], v[48:49], 0, s[36:37]
	v_lshl_add_u64 v[102:103], v[46:47], 0, s[36:37]
	v_lshl_add_u64 v[104:105], v[44:45], 0, s[36:37]
	v_lshl_add_u64 v[106:107], v[42:43], 0, s[36:37]
	v_lshl_add_u64 v[108:109], v[40:41], 0, s[36:37]
	v_lshl_add_u64 v[110:111], v[38:39], 0, s[36:37]
	v_lshl_add_u64 v[112:113], v[36:37], 0, s[36:37]
	global_load_dword v158, v[98:99], off nt
	s_nop 0
	global_load_dword v159, v[100:101], off nt
	global_load_dword v160, v[102:103], off nt
	s_nop 0
	global_load_dword v161, v[104:105], off nt
	global_load_dword v162, v[106:107], off nt
	global_load_dword v163, v[108:109], off nt
	global_load_dword v164, v[110:111], off nt
	s_nop 0
	global_load_dword v165, v[112:113], off nt
	s_add_u32 s36, s36, 0x4000
	s_addc_u32 s37, s37, 0
	v_add_u32_e32 v105, 0x400, v35
	s_waitcnt vmcnt(30)
	ds_write2_b32 v35, v134, v135 offset1:66
	s_waitcnt vmcnt(28)
	ds_write2_b32 v35, v136, v137 offset0:132 offset1:198
	s_waitcnt vmcnt(26)
	ds_write2_b32 v105, v138, v139 offset0:8 offset1:74
	s_waitcnt vmcnt(24)
; #define LAS __attribute__((address_space(3)))
; __device__ __forceinline__ unsigned pk2(float lo, float hi) { unsigned r; asm("v_cvt_pk_bf16_f32 %0, %1, %2" : "=v"(r) : "v"(lo), "v"(hi)); return r; }
; #define LDS_FENCE() asm volatile("s_waitcnt lgkmcnt(0)" ::: "memory")
;     ...
;     for (int i = 0; i < 32; ++i) { const int kk = 2 * i + (lane >> 5); scr[kk * 33 + (lane & 31)] = __builtin_nontemporal_load(W + (size_t)(k0 + kk) * ldw + n0 + (lane & 31)); }
;     LDS_FENCE();
;     const int c = lane & 7;
; #pragma unroll
;     for (int j = 0; j < 4; ++j) { const int n = (lane >> 3) + 8 * j; const LAS float* s = scr + (8 * c) * 33 + n;
;         v4u o; o.x = pk2(s[0 * 33], s[1 * 33]); o.y = pk2(s[2 * 33], s[3 * 33]); o.z = pk2(s[4 * 33], s[5 * 33]); o.w = pk2(s[6 * 33], s[7 * 33]);
;         int nr = n;
;         if (perm16) { const int cc = (n0 + n) & 255;
;             nr = (((cc >> 3) & 1) << 7) + ((cc >> 6) << 5) + (((cc >> 4) & 3) << 3) + (cc & 7) - (n0 & 255); }
;         if (fp8) {
;             v2u o8; o8.x = (unsigned)__builtin_amdgcn_cvt_pk_fp8_f32(s[2 * 33] * SW8, s[3 * 33] * SW8, __builtin_amdgcn_cvt_pk_fp8_f32(s[0 * 33] * SW8, s[1 * 33] * SW8, 0, false), true);
;             o8.y = (unsigned)__builtin_amdgcn_cvt_pk_fp8_f32(s[6 * 33] * SW8, s[7 * 33] * SW8, __builtin_amdgcn_cvt_pk_fp8_f32(s[4 * 33] * SW8, s[5 * 33] * SW8, 0, false), true);
;             *(v2u*)((unsigned char*)dst + (ptrdiff_t)nr * Kd + 8 * c) = o8;
;         } else *(v4u*)(dst + (ptrdiff_t)nr * Kd + 8 * c) = o; }
;     LDS_FENCE();
; __device__ __forceinline__ void phase_p0a(const Ptrs& P, LAS unsigned char* lds, int tid_, int vcu, int G) {
;     ...
;     for (int it = gw; it < NL * NI_L; it += NGW) {
	ds_write2_b32 v105, v140, v141 offset0:140 offset1:206
	v_add_u32_e32 v35, 0x840, v35
	v_add_u32_e32 v105, 0x400, v35
	s_waitcnt vmcnt(22)
	ds_write2_b32 v35, v142, v143 offset1:66
	s_waitcnt vmcnt(20)
	ds_write2_b32 v35, v144, v145 offset0:132 offset1:198
	s_waitcnt vmcnt(18)
	ds_write2_b32 v105, v146, v147 offset0:8 offset1:74
	s_waitcnt vmcnt(16)
	ds_write2_b32 v105, v148, v149 offset0:140 offset1:206
	v_add_u32_e32 v35, 0x840, v35
	v_add_u32_e32 v105, 0x400, v35
	s_waitcnt vmcnt(14)
	ds_write2_b32 v35, v150, v151 offset1:66
	s_waitcnt vmcnt(12)
	ds_write2_b32 v35, v152, v153 offset0:132 offset1:198
	s_waitcnt vmcnt(10)
	ds_write2_b32 v105, v154, v155 offset0:8 offset1:74
	s_waitcnt vmcnt(8)
	ds_write2_b32 v105, v156, v157 offset0:140 offset1:206
	v_add_u32_e32 v35, 0x840, v35
	v_add_u32_e32 v105, 0x400, v35
	s_waitcnt vmcnt(6)
	ds_write2_b32 v35, v158, v159 offset1:66
	s_waitcnt vmcnt(4)
	ds_write2_b32 v35, v160, v161 offset0:132 offset1:198
	s_waitcnt vmcnt(2)
	ds_write2_b32 v105, v162, v163 offset0:8 offset1:74
	s_waitcnt vmcnt(0)
	ds_write2_b32 v105, v164, v165 offset0:140 offset1:206
	v_add_u32_e32 v35, 0x840, v35
	s_cmp_lg_u32 s36, 0x10000
	v_add_u32_e32 v36, v94, v96
	v_mov_b32_e32 v37, v3
	v_mov_b64_e32 v[38:39], s[0:1]
	v_lshlrev_b64 v[36:37], 11, v[36:37]
	v_mad_u64_u32 v[38:39], s[36:37], v2, s55, v[38:39]
	s_waitcnt lgkmcnt(0)
	v_lshl_add_u64 v[36:37], v[38:39], 0, v[36:37]
	v_lshlrev_b32_e32 v2, 1, v95
	ds_read2_b32 v[40:41], v7 offset0:33 offset1:41
	ds_read2_b32 v[42:43], v7 offset1:8
	ds_read2_b32 v[44:45], v7 offset0:66 offset1:74
	ds_read2_b32 v[46:47], v7 offset0:99 offset1:107
	ds_read2_b32 v[48:49], v7 offset0:132 offset1:140
	ds_read2_b32 v[50:51], v7 offset0:165 offset1:173
	ds_read2_b32 v[94:95], v7 offset0:198 offset1:206
	ds_read2_b32 v[96:97], v7 offset0:231 offset1:239
	v_lshl_add_u64 v[36:37], v[36:37], 0, v[2:3]
	v_lshlrev_b32_e32 v2, 1, v4
	v_lshl_add_u64 v[36:37], v[36:37], 0, v[2:3]
	v_lshl_add_u64 v[98:99], v[36:37], 0, s[20:21]
	v_lshlrev_b32_e32 v2, 1, v6
	v_lshl_add_u64 v[100:101], v[98:99], 0, v[2:3]
	s_waitcnt lgkmcnt(6)
	v_cvt_pk_bf16_f32 v36, v42, v40
	s_waitcnt lgkmcnt(4)
	v_cvt_pk_bf16_f32 v37, v44, v46
	s_waitcnt lgkmcnt(2)
	v_cvt_pk_bf16_f32 v38, v48, v50
	s_waitcnt lgkmcnt(0)
	v_cvt_pk_bf16_f32 v39, v94, v96
	global_store_dwordx4 v[100:101], v[36:39], off
	v_lshlrev_b32_e32 v2, 1, v8
	s_nop 0
	v_cvt_pk_bf16_f32 v36, v43, v41
	v_cvt_pk_bf16_f32 v37, v45, v47
	v_cvt_pk_bf16_f32 v38, v49, v51
	v_cvt_pk_bf16_f32 v39, v95, v97
	ds_read2_b32 v[42:43], v7 offset0:16 offset1:24
	ds_read2_b32 v[44:45], v7 offset0:49 offset1:57
	ds_read2_b32 v[46:47], v7 offset0:82 offset1:90
	ds_read2_b32 v[48:49], v7 offset0:115 offset1:123
	ds_read2_b32 v[50:51], v7 offset0:148 offset1:156
	ds_read2_b32 v[94:95], v7 offset0:181 offset1:189
	ds_read2_b32 v[96:97], v7 offset0:214 offset1:222
	ds_read2_b32 v[100:101], v7 offset0:247 offset1:255
	v_lshl_add_u64 v[40:41], v[98:99], 0, v[2:3]
	v_lshlrev_b32_e32 v2, 1, v10
	global_store_dwordx4 v[40:41], v[36:39], off
	v_lshl_add_u64 v[40:41], v[98:99], 0, v[2:3]
	v_lshlrev_b32_e32 v2, 1, v12
	s_waitcnt lgkmcnt(6)
	v_cvt_pk_bf16_f32 v36, v42, v44
	s_waitcnt lgkmcnt(4)
	v_cvt_pk_bf16_f32 v37, v46, v48
	s_waitcnt lgkmcnt(2)
	v_cvt_pk_bf16_f32 v38, v50, v94
	s_waitcnt lgkmcnt(0)
	v_cvt_pk_bf16_f32 v39, v96, v100
	global_store_dwordx4 v[40:41], v[36:39], off
	v_lshl_add_u64 v[40:41], v[98:99], 0, v[2:3]
	s_nop 0
	v_cvt_pk_bf16_f32 v36, v43, v45
	v_cvt_pk_bf16_f32 v37, v47, v49
	v_cvt_pk_bf16_f32 v38, v51, v95
	v_cvt_pk_bf16_f32 v39, v97, v101
	global_store_dwordx4 v[40:41], v[36:39], off
	s_waitcnt lgkmcnt(0)
	s_branch .LBB0_45

; __device__ __forceinline__ void phase_m2(const Ptrs& P, int tid_, int vcu, int G) {
;     ...
;         for (int step = 0; step < 16; ++step) {
;             const int c = dir ? 15 - step : step; const size_t du = (size_t)dir * 512 + bh * 16 + c;
;             ml[step] = mg[du * 2]; gg[step] = mg[du * 2 + 1];
;             if (!small) loc[step] = __builtin_nontemporal_load((const f32x4*)(cloc + du * 8192 + blk * 2048) + tid);
;             else loc[step] = (f32x4){nloc[du * 64 + tid], 0.f, 0.f, 0.f};
;         }
.LBB0_537:
	s_andn2_b64 vcc, exec, s[8:9]
	s_cbranch_vccnz .LBB0_539
	s_lshl_b64 s[8:9], s[18:19], 8
	v_lshl_add_u64 v[4:5], v[64:65], 0, s[8:9]
	global_load_dword v58, v[4:5], off
	v_mov_b32_e32 v59, 0
	v_mov_b32_e32 v60, v59
	v_mov_b32_e32 v61, v59

; __device__ __forceinline__ void phase_m2(const Ptrs& P, int tid_, int vcu, int G) {
;     ...
;         for (int step = 0; step < 16; ++step) {
;             const int c = dir ? 15 - step : step; const size_t du = (size_t)dir * 512 + bh * 16 + c;
;             ml[step] = mg[du * 2]; gg[step] = mg[du * 2 + 1];
;             if (!small) loc[step] = __builtin_nontemporal_load((const f32x4*)(cloc + du * 8192 + blk * 2048) + tid);
;             else loc[step] = (f32x4){nloc[du * 64 + tid], 0.f, 0.f, 0.f};
;         }
.LBB0_541:
	s_andn2_b64 vcc, exec, s[8:9]
	s_cbranch_vccnz .LBB0_543
	s_lshl_b64 s[8:9], s[60:61], 8
	v_lshl_add_u64 v[4:5], v[64:65], 0, s[8:9]
	global_load_dword v54, v[4:5], off
	v_mov_b32_e32 v55, 0
	v_mov_b32_e32 v56, v55
	v_mov_b32_e32 v57, v55

; __device__ __forceinline__ void phase_m2(const Ptrs& P, int tid_, int vcu, int G) {
;     ...
;         for (int step = 0; step < 16; ++step) {
;             const int c = dir ? 15 - step : step; const size_t du = (size_t)dir * 512 + bh * 16 + c;
;             ml[step] = mg[du * 2]; gg[step] = mg[du * 2 + 1];
;             if (!small) loc[step] = __builtin_nontemporal_load((const f32x4*)(cloc + du * 8192 + blk * 2048) + tid);
;             else loc[step] = (f32x4){nloc[du * 64 + tid], 0.f, 0.f, 0.f};
;         }
.LBB0_545:
	s_andn2_b64 vcc, exec, s[28:29]
	s_cbranch_vccnz .LBB0_547
	s_lshl_b64 s[22:23], s[8:9], 8
	v_lshl_add_u64 v[4:5], v[64:65], 0, s[22:23]
	global_load_dword v50, v[4:5], off
	v_mov_b32_e32 v51, 0
	v_mov_b32_e32 v52, v51
	v_mov_b32_e32 v53, v51

; __device__ __forceinline__ void phase_m2(const Ptrs& P, int tid_, int vcu, int G) {
;     ...
;         for (int step = 0; step < 16; ++step) {
;             const int c = dir ? 15 - step : step; const size_t du = (size_t)dir * 512 + bh * 16 + c;
;             ml[step] = mg[du * 2]; gg[step] = mg[du * 2 + 1];
;             if (!small) loc[step] = __builtin_nontemporal_load((const f32x4*)(cloc + du * 8192 + blk * 2048) + tid);
;             else loc[step] = (f32x4){nloc[du * 64 + tid], 0.f, 0.f, 0.f};
;         }
.LBB0_549:
	s_andn2_b64 vcc, exec, s[28:29]
	s_cbranch_vccnz .LBB0_551
	s_lshl_b64 s[22:23], s[34:35], 8
	v_lshl_add_u64 v[4:5], v[64:65], 0, s[22:23]
	global_load_dword v46, v[4:5], off
	v_mov_b32_e32 v47, 0
	v_mov_b32_e32 v48, v47
	v_mov_b32_e32 v49, v47

; __device__ __forceinline__ void phase_m2(const Ptrs& P, int tid_, int vcu, int G) {
;     ...
;         for (int step = 0; step < 16; ++step) {
;             const int c = dir ? 15 - step : step; const size_t du = (size_t)dir * 512 + bh * 16 + c;
;             ml[step] = mg[du * 2]; gg[step] = mg[du * 2 + 1];
;             if (!small) loc[step] = __builtin_nontemporal_load((const f32x4*)(cloc + du * 8192 + blk * 2048) + tid);
;             else loc[step] = (f32x4){nloc[du * 64 + tid], 0.f, 0.f, 0.f};
;         }
.LBB0_553:
	s_andn2_b64 vcc, exec, s[28:29]
	s_cbranch_vccnz .LBB0_555
	s_lshl_b64 s[22:23], s[92:93], 8
	v_lshl_add_u64 v[4:5], v[64:65], 0, s[22:23]
	global_load_dword v42, v[4:5], off
	v_mov_b32_e32 v43, 0
	v_mov_b32_e32 v44, v43
	v_mov_b32_e32 v45, v43

; __device__ __forceinline__ void phase_m2(const Ptrs& P, int tid_, int vcu, int G) {
;     ...
;         for (int step = 0; step < 16; ++step) {
;             const int c = dir ? 15 - step : step; const size_t du = (size_t)dir * 512 + bh * 16 + c;
;             ml[step] = mg[du * 2]; gg[step] = mg[du * 2 + 1];
;             if (!small) loc[step] = __builtin_nontemporal_load((const f32x4*)(cloc + du * 8192 + blk * 2048) + tid);
;             else loc[step] = (f32x4){nloc[du * 64 + tid], 0.f, 0.f, 0.f};
;         }
.LBB0_557:
	s_andn2_b64 vcc, exec, s[28:29]
	s_cbranch_vccnz .LBB0_559
	s_lshl_b64 s[22:23], s[90:91], 8
	v_lshl_add_u64 v[4:5], v[64:65], 0, s[22:23]
	global_load_dword v38, v[4:5], off
	v_mov_b32_e32 v39, 0
	v_mov_b32_e32 v40, v39
	v_mov_b32_e32 v41, v39

; __device__ __forceinline__ void phase_m2(const Ptrs& P, int tid_, int vcu, int G) {
;     ...
;         for (int step = 0; step < 16; ++step) {
;             const int c = dir ? 15 - step : step; const size_t du = (size_t)dir * 512 + bh * 16 + c;
;             ml[step] = mg[du * 2]; gg[step] = mg[du * 2 + 1];
;             if (!small) loc[step] = __builtin_nontemporal_load((const f32x4*)(cloc + du * 8192 + blk * 2048) + tid);
;             else loc[step] = (f32x4){nloc[du * 64 + tid], 0.f, 0.f, 0.f};
;         }
.LBB0_561:
	s_andn2_b64 vcc, exec, s[28:29]
	s_cbranch_vccnz .LBB0_563
	s_lshl_b64 s[22:23], s[66:67], 8
	v_lshl_add_u64 v[4:5], v[64:65], 0, s[22:23]
	global_load_dword v34, v[4:5], off
	v_mov_b32_e32 v35, 0
	v_mov_b32_e32 v36, v35
	v_mov_b32_e32 v37, v35

; __device__ __forceinline__ void phase_m2(const Ptrs& P, int tid_, int vcu, int G) {
;     ...
;         for (int step = 0; step < 16; ++step) {
;             const int c = dir ? 15 - step : step; const size_t du = (size_t)dir * 512 + bh * 16 + c;
;             ml[step] = mg[du * 2]; gg[step] = mg[du * 2 + 1];
;             if (!small) loc[step] = __builtin_nontemporal_load((const f32x4*)(cloc + du * 8192 + blk * 2048) + tid);
;             else loc[step] = (f32x4){nloc[du * 64 + tid], 0.f, 0.f, 0.f};
;         }
.LBB0_565:
	s_andn2_b64 vcc, exec, s[28:29]
	s_cbranch_vccnz .LBB0_567
	s_lshl_b64 s[22:23], s[64:65], 8
	v_lshl_add_u64 v[4:5], v[64:65], 0, s[22:23]
	global_load_dword v30, v[4:5], off
	v_mov_b32_e32 v31, 0
	v_mov_b32_e32 v32, v31
	v_mov_b32_e32 v33, v31

; __device__ __forceinline__ void phase_m2(const Ptrs& P, int tid_, int vcu, int G) {
;     ...
;         for (int step = 0; step < 16; ++step) {
;             const int c = dir ? 15 - step : step; const size_t du = (size_t)dir * 512 + bh * 16 + c;
;             ml[step] = mg[du * 2]; gg[step] = mg[du * 2 + 1];
;             if (!small) loc[step] = __builtin_nontemporal_load((const f32x4*)(cloc + du * 8192 + blk * 2048) + tid);
;             else loc[step] = (f32x4){nloc[du * 64 + tid], 0.f, 0.f, 0.f};
;         }
.LBB0_569:
	s_andn2_b64 vcc, exec, s[28:29]
	s_cbranch_vccnz .LBB0_571
	s_lshl_b64 s[22:23], s[54:55], 8
	v_lshl_add_u64 v[4:5], v[64:65], 0, s[22:23]
	global_load_dword v26, v[4:5], off
	v_mov_b32_e32 v27, 0
	v_mov_b32_e32 v28, v27
	v_mov_b32_e32 v29, v27

; __device__ __forceinline__ void phase_m2(const Ptrs& P, int tid_, int vcu, int G) {
;     ...
;         for (int step = 0; step < 16; ++step) {
;             const int c = dir ? 15 - step : step; const size_t du = (size_t)dir * 512 + bh * 16 + c;
;             ml[step] = mg[du * 2]; gg[step] = mg[du * 2 + 1];
;             if (!small) loc[step] = __builtin_nontemporal_load((const f32x4*)(cloc + du * 8192 + blk * 2048) + tid);
;             else loc[step] = (f32x4){nloc[du * 64 + tid], 0.f, 0.f, 0.f};
;         }
.LBB0_573:
	s_andn2_b64 vcc, exec, s[28:29]
	s_cbranch_vccnz .LBB0_575
	s_lshl_b64 s[22:23], s[50:51], 8
	v_lshl_add_u64 v[4:5], v[64:65], 0, s[22:23]
	global_load_dword v22, v[4:5], off
	v_mov_b32_e32 v23, 0
	v_mov_b32_e32 v24, v23
	v_mov_b32_e32 v25, v23

; __device__ __forceinline__ void phase_m2(const Ptrs& P, int tid_, int vcu, int G) {
;     ...
;         for (int step = 0; step < 16; ++step) {
;             const int c = dir ? 15 - step : step; const size_t du = (size_t)dir * 512 + bh * 16 + c;
;             ml[step] = mg[du * 2]; gg[step] = mg[du * 2 + 1];
;             if (!small) loc[step] = __builtin_nontemporal_load((const f32x4*)(cloc + du * 8192 + blk * 2048) + tid);
;             else loc[step] = (f32x4){nloc[du * 64 + tid], 0.f, 0.f, 0.f};
;         }
.LBB0_577:
	s_andn2_b64 vcc, exec, s[28:29]
	s_cbranch_vccnz .LBB0_579
	s_lshl_b64 s[22:23], s[48:49], 8
	v_lshl_add_u64 v[4:5], v[64:65], 0, s[22:23]
	global_load_dword v18, v[4:5], off
	v_mov_b32_e32 v19, 0
	v_mov_b32_e32 v20, v19
	v_mov_b32_e32 v21, v19

; __device__ __forceinline__ void phase_m2(const Ptrs& P, int tid_, int vcu, int G) {
;     ...
;         for (int step = 0; step < 16; ++step) {
;             const int c = dir ? 15 - step : step; const size_t du = (size_t)dir * 512 + bh * 16 + c;
;             ml[step] = mg[du * 2]; gg[step] = mg[du * 2 + 1];
;             if (!small) loc[step] = __builtin_nontemporal_load((const f32x4*)(cloc + du * 8192 + blk * 2048) + tid);
;             else loc[step] = (f32x4){nloc[du * 64 + tid], 0.f, 0.f, 0.f};
;         }
.LBB0_581:
	s_andn2_b64 vcc, exec, s[28:29]
	s_cbranch_vccnz .LBB0_583
	s_lshl_b64 s[22:23], s[46:47], 8
	v_lshl_add_u64 v[4:5], v[64:65], 0, s[22:23]
	global_load_dword v14, v[4:5], off
	v_mov_b32_e32 v15, 0
	v_mov_b32_e32 v16, v15
	v_mov_b32_e32 v17, v15

; __device__ __forceinline__ void phase_m2(const Ptrs& P, int tid_, int vcu, int G) {
;     ...
;         for (int step = 0; step < 16; ++step) {
;             const int c = dir ? 15 - step : step; const size_t du = (size_t)dir * 512 + bh * 16 + c;
;             ml[step] = mg[du * 2]; gg[step] = mg[du * 2 + 1];
;             if (!small) loc[step] = __builtin_nontemporal_load((const f32x4*)(cloc + du * 8192 + blk * 2048) + tid);
;             else loc[step] = (f32x4){nloc[du * 64 + tid], 0.f, 0.f, 0.f};
;         }
.LBB0_585:
	s_andn2_b64 vcc, exec, s[28:29]
	s_cbranch_vccnz .LBB0_587
	s_lshl_b64 s[22:23], s[44:45], 8
	v_lshl_add_u64 v[4:5], v[64:65], 0, s[22:23]
	global_load_dword v10, v[4:5], off
	v_mov_b32_e32 v11, 0
	v_mov_b32_e32 v12, v11
	v_mov_b32_e32 v13, v11

; __device__ __forceinline__ void phase_m2(const Ptrs& P, int tid_, int vcu, int G) {
;     ...
;         for (int step = 0; step < 16; ++step) {
;             const int c = dir ? 15 - step : step; const size_t du = (size_t)dir * 512 + bh * 16 + c;
;             ml[step] = mg[du * 2]; gg[step] = mg[du * 2 + 1];
;             if (!small) loc[step] = __builtin_nontemporal_load((const f32x4*)(cloc + du * 8192 + blk * 2048) + tid);
;             else loc[step] = (f32x4){nloc[du * 64 + tid], 0.f, 0.f, 0.f};
;         }
.LBB0_589:
	s_andn2_b64 vcc, exec, s[28:29]
	s_cbranch_vccnz .LBB0_591
	s_lshl_b64 s[22:23], s[30:31], 8
	v_lshl_add_u64 v[4:5], v[64:65], 0, s[22:23]
	global_load_dword v6, v[4:5], off
	v_mov_b32_e32 v7, 0
	v_mov_b32_e32 v8, v7
	v_mov_b32_e32 v9, v7

; __device__ __forceinline__ void phase_m2(const Ptrs& P, int tid_, int vcu, int G) {
;     ...
;         for (int step = 0; step < 16; ++step) {
;             const int c = dir ? 15 - step : step; const size_t du = (size_t)dir * 512 + bh * 16 + c;
;             ml[step] = mg[du * 2]; gg[step] = mg[du * 2 + 1];
;             if (!small) loc[step] = __builtin_nontemporal_load((const f32x4*)(cloc + du * 8192 + blk * 2048) + tid);
;             else loc[step] = (f32x4){nloc[du * 64 + tid], 0.f, 0.f, 0.f};
;         }
.LBB0_593:
	s_andn2_b64 vcc, exec, s[62:63]
	s_cbranch_vccnz .LBB0_595
	s_lshl_b64 s[22:23], s[28:29], 8
	v_lshl_add_u64 v[2:3], v[64:65], 0, s[22:23]
	global_load_dword v2, v[2:3], off
	v_mov_b32_e32 v3, 0
	v_mov_b32_e32 v4, v3
	v_mov_b32_e32 v5, v3

; __device__ __forceinline__ unsigned pk2(float lo, float hi) { unsigned r; asm("v_cvt_pk_bf16_f32 %0, %1, %2" : "=v"(r) : "v"(lo), "v"(hi)); return r; }
; __device__ __forceinline__ float bf2f(unsigned b) { return __uint_as_float(b << 16); }
; __device__ __forceinline__ float bflo(unsigned w) { return __uint_as_float(w << 16); }
; __device__ __forceinline__ float bfhi(unsigned w) { return __uint_as_float(w & 0xffff0000u); }
; __device__ __forceinline__ void phase_pqfold(const Ptrs& P, int tid_, int vcu, int G) {
;     ...
;     for (size_t i = gt; i < (size_t)2048 * 2048 / 8; i += NGT) { const int row = (int)(i >> 8), k8 = (int)(i & 255) * 8; const bool sinpart = k8 >= 1024; const int s8 = k8 & 1023;
;         const bf16* src = PQ + (size_t)row * 4096 + (sinpart ? 2048 : 0);
;         const v4u f = *(const v4u*)(src + s8); const unsigned fw[4] = {f.x, f.y, f.z, f.w}; float v[8];
; #pragma unroll
;         for (int j = 0; j < 8; ++j) { const int sx = s8 + j; const float a = (j & 1) ? bfhi(fw[j >> 1]) : bflo(fw[j >> 1]); const float r = (sx > 0) ? bf2f(src[2048 - sx]) : 0.f;
;             v[j] = sinpart ? ((sx > 0) ? a - r : bf2f(PQ[(size_t)row * 4096 + 1024])) : a + r; }
;         v4u w; w.x = pk2(v[0], v[1]); w.y = pk2(v[2], v[3]); w.z = pk2(v[4], v[5]); w.w = pk2(v[6], v[7]); ((v4u*)PF)[i] = w; }
.LBB0_692:
	s_or_b64 exec, exec, s[18:19]
	v_and_b32_e32 v2, 0xffff0000, v2
	v_lshlrev_b32_e32 v13, 16, v3
	v_and_b32_e32 v3, 0xffff0000, v3
	v_lshl_add_u64 v[6:7], v[6:7], 0, s[24:25]
	s_mov_b64 s[4:5], 0x7ffff
	v_add_u32_e32 v1, s36, v1
	s_waitcnt vmcnt(0)
	v_lshlrev_b32_e32 v12, 16, v110
	v_cndmask_b32_e64 v12, -v12, v12, vcc
	v_add_f32_e32 v2, v12, v2
	v_cvt_pk_bf16_f32 v2, v14, v2
	s_waitcnt vmcnt(0)
	v_and_b32_e32 v15, 0xffff0000, v114
	v_cndmask_b32_e64 v15, -v15, v15, vcc
	v_lshlrev_b32_e32 v12, 16, v114
	v_add_f32_e32 v13, v15, v13
	v_cndmask_b32_e64 v12, -v12, v12, vcc
	v_and_b32_e32 v15, 0xffff0000, v113
	v_add_f32_e32 v3, v12, v3
	v_lshlrev_b32_e32 v12, 16, v4
	v_cndmask_b32_e64 v15, -v15, v15, vcc
	v_lshlrev_b32_e32 v11, 16, v113
	v_add_f32_e32 v12, v15, v12
	v_and_b32_e32 v4, 0xffff0000, v4
	v_cndmask_b32_e64 v11, -v11, v11, vcc
	v_and_b32_e32 v15, 0xffff0000, v112
	v_lshlrev_b32_e32 v10, 16, v112
	v_add_f32_e32 v4, v11, v4
	v_lshlrev_b32_e32 v11, 16, v5
	v_cndmask_b32_e64 v15, -v15, v15, vcc
	v_and_b32_e32 v5, 0xffff0000, v5
	v_cndmask_b32_e64 v10, -v10, v10, vcc
	v_add_f32_e32 v11, v15, v11
	v_add_f32_e32 v5, v10, v5
	v_cmp_lt_u64_e32 vcc, s[4:5], v[6:7]
	v_cvt_pk_bf16_f32 v5, v11, v5
	v_lshl_add_u64 v[10:11], s[0:1], 0, v[8:9]
	v_lshl_add_u64 v[8:9], v[8:9], 0, s[28:29]
	s_or_b64 s[12:13], vcc, s[12:13]
	v_cvt_pk_bf16_f32 v3, v13, v3
	v_cvt_pk_bf16_f32 v4, v12, v4
	global_store_dwordx4 v[10:11], v[2:5], off
	s_andn2_b64 exec, exec, s[12:13]
	s_cbranch_execz .LBB0_703
.LBB0_693:
	v_and_b32_e32 v2, 0x7ff000, v8
	v_and_b32_e32 v14, 0x80, v6
	v_lshlrev_b32_e32 v162, 1, v2
	v_and_b32_e32 v15, 0x3f8, v1
	v_lshl_add_u64 v[12:13], s[8:9], 0, v[162:163]
	v_lshlrev_b32_e32 v162, 5, v14
	v_lshl_add_u64 v[10:11], v[12:13], 0, v[162:163]
	v_lshlrev_b32_e32 v162, 1, v15
	v_lshl_add_u64 v[2:3], v[10:11], 0, v[162:163]
	global_load_dwordx4 v[2:5], v[2:3], off
	v_xor_b32_e32 v110, 0x3f8, v15
	v_lshlrev_b32_e32 v162, 1, v110
	v_lshl_add_u64 v[110:111], v[10:11], 0, v[162:163]
	global_load_ushort v110, v[110:111], off offset:2062
	v_sub_u32_e32 v112, 0x7f9, v15
	v_lshlrev_b32_e32 v162, 1, v112
	v_lshl_add_u64 v[112:113], v[10:11], 0, v[162:163]
	global_load_dwordx3 v[112:114], v[112:113], off
	v_cmp_ne_u32_e64 s[38:39], 0, v15
	v_mov_b32_e32 v16, 0
	s_and_saveexec_b64 s[18:19], s[38:39]
	s_cbranch_execz .LBB0_695
	v_sub_u32_e32 v16, 0x800, v15
	v_lshlrev_b32_e32 v162, 1, v16
	v_lshl_add_u64 v[16:17], v[10:11], 0, v[162:163]
	global_load_ushort v16, v[16:17], off
	s_waitcnt vmcnt(0)
	v_lshlrev_b32_e32 v16, 16, v16

; __device__ __forceinline__ float bflo(unsigned w) { return __uint_as_float(w << 16); }
; __device__ __forceinline__ float bfhi(unsigned w) { return __uint_as_float(w & 0xffff0000u); }
; __device__ __forceinline__ void phase_combine(const Ptrs& P, int tid_, int vcu, int G) {
;     ...
;     for (int t = gw; t < T; t += NGW) {
;         float v[16]; v4u ys[2], yk[8];
;         const v4u* hp = (const v4u*)(H + (size_t)t * D) + 2 * lane; const v4u* ysp = (const v4u*)(YS + (size_t)t * D) + 2 * lane; const v4u* yr = (const v4u*)(Y8 + (size_t)t * 8 * 1024) + lane;
;         float mg = 0.f; if (lane < 8) mg = tg[(size_t)t * 8 + lane] * (1.f / 16.f);
; #pragma unroll
;         for (int q = 0; q < 2; ++q) { const v4u a = hp[q]; v[8 * q] = bflo(a.x); v[8 * q + 1] = bfhi(a.x); v[8 * q + 2] = bflo(a.y); v[8 * q + 3] = bfhi(a.y); v[8 * q + 4] = bflo(a.z); v[8 * q + 5] = bfhi(a.z); v[8 * q + 6] = bflo(a.w); v[8 * q + 7] = bfhi(a.w); }
;         ys[0] = __builtin_nontemporal_load(ysp); ys[1] = __builtin_nontemporal_load(ysp + 1);
; #pragma unroll
;         for (int k = 0; k < 8; ++k) yk[k] = __builtin_nontemporal_load(yr + k * 64);
.LBB0_1438:
	s_andn2_b64 vcc, exec, s[0:1]
	s_cbranch_vccnz .LBB0_1498
	s_mov_b64 s[6:7], s[76:77]
	s_waitcnt lgkmcnt(0)
	v_mov_b32_e32 v3, v0
	v_readlane_b32 s0, v254, 63
	v_ashrrev_i32_e32 v2, 6, v3
	v_readlane_b32 s1, v255, 0
	v_add_u32_e32 v1, s0, v2
	s_movk_i32 s0, 0x4000
	v_cmp_gt_i32_e32 vcc, s0, v1
	s_and_saveexec_b64 s[0:1], vcc
	s_cbranch_execz .LBB0_1444
	v_readlane_b32 s4, v254, 63
	s_load_dwordx2 s[6:7], s[6:7], 0xd8
	s_waitcnt vmcnt(0)
	v_and_b32_e32 v6, 63, v3
	v_ashrrev_i32_e32 v3, 31, v2
	v_readlane_b32 s5, v255, 0
	v_lshlrev_b32_e32 v162, 2, v6
	v_cmp_gt_u32_e64 s[38:39], 8, v6
	v_lshl_add_u64 v[2:3], s[4:5], 0, v[2:3]
	v_lshlrev_b64 v[4:5], 5, v[2:3]
	v_lshl_add_u64 v[4:5], v[4:5], 0, v[162:163]
	s_mov_b64 s[4:5], 0x59000000
	v_lshlrev_b64 v[32:33], 13, v[2:3]
	v_lshlrev_b64 v[34:35], 11, v[2:3]
	v_lshl_add_u64 v[30:31], v[4:5], 0, s[4:5]
	v_lshl_or_b32 v32, v6, 4, v32
	v_lshl_or_b32 v34, v6, 5, v34
	s_mov_b64 s[12:13], 0
	s_waitcnt lgkmcnt(0)
	v_mov_b32_e32 v232, 0
	s_and_saveexec_b64 s[8:9], s[38:39]
	v_lshl_add_u64 v[240:241], s[6:7], 0, v[30:31]
	global_load_dword v232, v[240:241], off
	s_or_b64 exec, exec, s[8:9]
	v_lshl_add_u64 v[240:241], s[6:7], 0, v[34:35]
	v_add_co_u32_e32 v242, vcc, 0x34600000, v240
	s_nop 1
	v_addc_co_u32_e32 v243, vcc, 0, v241, vcc
	global_load_dwordx4 v[180:183], v[242:243], off
	global_load_dwordx4 v[184:187], v[242:243], off offset:16
	v_add_co_u32_e32 v242, vcc, 0x3a600000, v240
	s_nop 1
	v_addc_co_u32_e32 v243, vcc, 0, v241, vcc
	global_load_dwordx4 v[188:191], v[242:243], off nt
	global_load_dwordx4 v[192:195], v[242:243], off offset:16 nt
	v_lshl_add_u64 v[240:241], s[6:7], 0, v[32:33]
	v_add_co_u32_e32 v242, vcc, 0x3c600000, v240
	s_nop 1
	v_addc_co_u32_e32 v243, vcc, 0, v241, vcc
	global_load_dwordx4 v[200:203], v[242:243], off nt
	global_load_dwordx4 v[204:207], v[242:243], off offset:1024 nt
	global_load_dwordx4 v[208:211], v[242:243], off offset:2048 nt
	global_load_dwordx4 v[212:215], v[242:243], off offset:3072 nt
	v_add_co_u32_e32 v242, vcc, 0x3c601000, v240
	s_nop 1
	v_addc_co_u32_e32 v243, vcc, 0, v241, vcc
	global_load_dwordx4 v[216:219], v[242:243], off nt
	global_load_dwordx4 v[220:223], v[242:243], off offset:1024 nt
	global_load_dwordx4 v[224:227], v[242:243], off offset:2048 nt
	global_load_dwordx4 v[228:231], v[242:243], off offset:3072 nt
	s_waitcnt vmcnt(0)
	s_branch .LBB0_1442
.Lcomb_body:
	v_lshlrev_b32_e32 v105, 16, v40
	v_lshlrev_b32_e32 v114, 16, v46
	v_and_b32_e32 v111, 0xffff0000, v46
	v_lshlrev_b32_e32 v110, 16, v47
	v_and_b32_e32 v107, 0xffff0000, v47
	v_lshlrev_b32_e32 v106, 16, v48
	v_and_b32_e32 v103, 0xffff0000, v48
	v_lshlrev_b32_e32 v102, 16, v49
	v_and_b32_e32 v99, 0xffff0000, v49
	v_lshlrev_b32_e32 v96, 16, v42
	v_lshlrev_b32_e32 v97, 16, v50
	v_and_b32_e32 v94, 0xffff0000, v50
	v_and_b32_e32 v95, 0xffff0000, v42
	v_lshlrev_b32_e32 v92, 16, v43
	v_lshlrev_b32_e32 v93, 16, v51
	v_and_b32_e32 v90, 0xffff0000, v51
	v_and_b32_e32 v91, 0xffff0000, v43
	v_lshlrev_b32_e32 v88, 16, v44
	v_lshlrev_b32_e32 v89, 16, v52
	v_and_b32_e32 v86, 0xffff0000, v52
	v_and_b32_e32 v87, 0xffff0000, v44
	v_lshlrev_b32_e32 v84, 16, v45
	v_lshlrev_b32_e32 v85, 16, v53
	v_and_b32_e32 v82, 0xffff0000, v53
	v_and_b32_e32 v83, 0xffff0000, v45
	v_cvt_pk_f32_fp8_e32 v[50:51], v54
	v_cvt_pk_f32_fp8_sdwa v[48:49], v54 src0_sel:WORD_1
	v_cvt_pk_f32_fp8_e32 v[46:47], v55
	v_cvt_pk_f32_fp8_sdwa v[44:45], v55 src0_sel:WORD_1
	v_cvt_pk_f32_fp8_e32 v[42:43], v56
	v_cvt_pk_f32_fp8_sdwa v[64:65], v57 src0_sel:WORD_1
	v_cvt_pk_f32_fp8_e32 v[52:53], v26
	v_cvt_pk_f32_fp8_sdwa v[54:55], v26 src0_sel:WORD_1
	v_cvt_pk_f32_fp8_e32 v[68:69], v27
	v_cvt_pk_f32_fp8_sdwa v[70:71], v27 src0_sel:WORD_1
	v_cvt_pk_f32_fp8_e32 v[72:73], v28
	v_cvt_pk_f32_fp8_sdwa v[74:75], v28 src0_sel:WORD_1
	v_cvt_pk_f32_fp8_e32 v[76:77], v29
	v_cvt_pk_f32_fp8_sdwa v[28:29], v29 src0_sel:WORD_1
	v_and_b32_e32 v104, 0xffff0000, v40
	v_lshlrev_b32_e32 v101, 16, v41
	v_and_b32_e32 v100, 0xffff0000, v41
	v_cvt_pk_f32_fp8_sdwa v[40:41], v56 src0_sel:WORD_1
	v_lshlrev_b32_e32 v113, 16, v38
	v_and_b32_e32 v112, 0xffff0000, v38
	v_lshlrev_b32_e32 v109, 16, v39
	v_and_b32_e32 v108, 0xffff0000, v39
	v_cvt_pk_f32_fp8_e32 v[38:39], v57
	v_mov_b32_e32 v26, v64
	v_mov_b32_e32 v27, v28
	v_mov_b32_e32 v56, v50
	v_mov_b32_e32 v57, v52
	v_mov_b32_e32 v52, v51
	v_mov_b32_e32 v50, v48
	v_mov_b32_e32 v51, v54
	v_mov_b32_e32 v54, v49
	v_mov_b32_e32 v48, v46
	v_mov_b32_e32 v49, v68
	v_mov_b32_e32 v68, v47
	v_mov_b32_e32 v46, v44
	v_mov_b32_e32 v47, v70
	v_mov_b32_e32 v70, v45
	v_mov_b32_e32 v45, v72
	v_mov_b32_e32 v72, v43
	v_mov_b32_e32 v28, v65
	v_cvt_pk_f32_fp8_e32 v[64:65], v22
	v_cvt_pk_f32_fp8_e32 v[116:117], v24
	v_cvt_pk_f32_fp8_sdwa v[118:119], v24 src0_sel:WORD_1
	v_cvt_pk_f32_fp8_e32 v[120:121], v25
	v_cvt_pk_f32_fp8_sdwa v[122:123], v25 src0_sel:WORD_1
	v_cvt_pk_f32_fp8_e32 v[24:25], v18
	v_pk_mul_f32 v[62:63], v[52:53], s[8:9]
	v_pk_mul_f32 v[58:59], v[54:55], s[8:9]
	v_pk_mul_f32 v[54:55], v[68:69], s[8:9]
	v_pk_mul_f32 v[52:53], v[46:47], s[8:9]
	v_mov_b32_e32 v44, v42
	v_pk_mul_f32 v[46:47], v[72:73], s[8:9]
	v_mov_b32_e32 v42, v40
	v_mov_b32_e32 v43, v74
	v_mov_b32_e32 v74, v41
	v_cvt_pk_f32_fp8_sdwa v[68:69], v22 src0_sel:WORD_1
	v_cvt_pk_f32_fp8_sdwa v[72:73], v18 src0_sel:WORD_1
	v_pk_mul_f32 v[66:67], v[56:57], s[8:9]
	v_pk_mul_f32 v[60:61], v[50:51], s[8:9]
	v_pk_mul_f32 v[56:57], v[48:49], s[8:9]
	v_pk_mul_f32 v[50:51], v[70:71], s[8:9]
	v_pk_mul_f32 v[48:49], v[44:45], s[8:9]
	v_pk_mul_f32 v[44:45], v[42:43], s[8:9]
	v_pk_mul_f32 v[42:43], v[74:75], s[8:9]
	v_cvt_pk_f32_fp8_e32 v[70:71], v23
	v_cvt_pk_f32_fp8_e32 v[74:75], v19
; __device__ __forceinline__ void phase_combine(const Ptrs& P, int tid_, int vcu, int G) {
;     ...
;         for (int k = 0; k < 8; ++k) { const float g = __int_as_float(__builtin_amdgcn_readlane(__float_as_int(mg), k)); const unsigned w[4] = {yk[k].x, yk[k].y, yk[k].z, yk[k].w};
; #pragma unroll
;             for (int i = 0; i < 4; ++i) { const auto lo = __builtin_amdgcn_cvt_pk_f32_fp8((int)w[i], false); const auto hi = __builtin_amdgcn_cvt_pk_f32_fp8((int)w[i], true);
;                 v[4 * i] += g * lo[0]; v[4 * i + 1] += g * lo[1]; v[4 * i + 2] += g * hi[0]; v[4 * i + 3] += g * hi[1]; } }
	v_mov_b32_e32 v40, v38
	v_mov_b32_e32 v41, v76
	v_mov_b32_e32 v76, v39
	v_cvt_pk_f32_fp8_sdwa v[22:23], v23 src0_sel:WORD_1
	v_cvt_pk_f32_fp8_sdwa v[124:125], v19 src0_sel:WORD_1
	v_cvt_pk_f32_fp8_e32 v[126:127], v20
	v_pk_mul_f32 v[26:27], v[26:27], s[8:9]
	v_pk_mul_f32 v[40:41], v[40:41], s[8:9]
	v_pk_mul_f32 v[38:39], v[76:77], s[8:9]
	v_pk_mul_f32 v[28:29], v[28:29], s[8:9]
	v_readlane_b32 s8, v98, 2
	v_readlane_b32 s9, v98, 3
	v_cvt_pk_f32_fp8_sdwa v[128:129], v20 src0_sel:WORD_1
	v_mov_b32_e32 v77, v24
	v_mov_b32_e32 v24, v65
	v_cvt_pk_f32_fp8_e32 v[130:131], v21
	v_pk_mul_f32 v[134:135], v[24:25], s[8:9]
	v_mov_b32_e32 v24, v68
	v_mov_b32_e32 v25, v72
	v_pk_mul_f32 v[136:137], v[24:25], s[8:9]
	v_mov_b32_e32 v24, v70
	v_mov_b32_e32 v25, v74
	v_mov_b32_e32 v72, v69
	v_pk_mul_f32 v[80:81], v[24:25], s[8:9]
	v_mov_b32_e32 v24, v22
	v_mov_b32_e32 v25, v124
	v_mov_b32_e32 v124, v23
	v_mov_b32_e32 v22, v116
	v_mov_b32_e32 v23, v126
	v_cvt_pk_f32_fp8_sdwa v[20:21], v21 src0_sel:WORD_1
	v_pk_mul_f32 v[138:139], v[72:73], s[8:9]
	v_pk_mul_f32 v[72:73], v[22:23], s[8:9]
	v_mov_b32_e32 v22, v118
	v_mov_b32_e32 v23, v128
	v_mov_b32_e32 v128, v119
	v_mov_b32_e32 v76, v64
	v_mov_b32_e32 v126, v117
	v_pk_mul_f32 v[68:69], v[22:23], s[8:9]
	v_pk_mul_f32 v[64:65], v[128:129], s[8:9]
	v_mov_b32_e32 v22, v120
	v_mov_b32_e32 v23, v130
	v_mov_b32_e32 v130, v121
	v_cvt_pk_f32_fp8_e32 v[116:117], v14
	v_cvt_pk_f32_fp8_e32 v[128:129], v10
	v_pk_mul_f32 v[132:133], v[76:77], s[8:9]
	v_pk_mul_f32 v[76:77], v[24:25], s[8:9]
	v_pk_mul_f32 v[24:25], v[22:23], s[8:9]
	v_pk_mul_f32 v[22:23], v[130:131], s[8:9]
	v_cvt_pk_f32_fp8_sdwa v[118:119], v14 src0_sel:WORD_1
	v_cvt_pk_f32_fp8_sdwa v[130:131], v10 src0_sel:WORD_1
	v_mov_b32_e32 v74, v71
	v_cvt_pk_f32_fp8_e32 v[120:121], v15
	v_cvt_pk_f32_fp8_e32 v[140:141], v11
	v_cvt_pk_f32_fp8_e32 v[170:171], v4
	v_cvt_pk_f32_fp8_sdwa v[172:173], v4 src0_sel:WORD_1
	v_cvt_pk_f32_fp8_e32 v[174:175], v5
	v_cvt_pk_f32_fp8_sdwa v[4:5], v5 src0_sel:WORD_1
	v_mov_b32_e32 v18, v122
	v_mov_b32_e32 v19, v20
	v_pk_mul_f32 v[78:79], v[74:75], s[8:9]
	v_pk_mul_f32 v[74:75], v[124:125], s[8:9]
	v_pk_mul_f32 v[70:71], v[126:127], s[8:9]
	v_mov_b32_e32 v20, v123
	v_cvt_pk_f32_fp8_sdwa v[14:15], v15 src0_sel:WORD_1
	v_cvt_pk_f32_fp8_e32 v[122:123], v16
	v_cvt_pk_f32_fp8_sdwa v[124:125], v16 src0_sel:WORD_1
	v_cvt_pk_f32_fp8_e32 v[126:127], v17
	v_cvt_pk_f32_fp8_sdwa v[16:17], v17 src0_sel:WORD_1
	v_cvt_pk_f32_fp8_sdwa v[142:143], v11 src0_sel:WORD_1
	v_cvt_pk_f32_fp8_e32 v[144:145], v12
	v_cvt_pk_f32_fp8_sdwa v[146:147], v12 src0_sel:WORD_1
	v_cvt_pk_f32_fp8_e32 v[148:149], v13
	v_cvt_pk_f32_fp8_sdwa v[12:13], v13 src0_sel:WORD_1
	v_pk_mul_f32 v[18:19], v[18:19], s[8:9]
	v_pk_mul_f32 v[20:21], v[20:21], s[8:9]
	v_readlane_b32 s8, v98, 4
	v_readlane_b32 s9, v98, 5
	v_mov_b32_e32 v151, v128
	v_mov_b32_e32 v128, v117
	v_mov_b32_e32 v150, v116
	v_pk_mul_f32 v[116:117], v[128:129], s[8:9]
	v_mov_b32_e32 v129, v130
	v_mov_b32_e32 v130, v119
	v_mov_b32_e32 v128, v118
	v_pk_mul_f32 v[118:119], v[130:131], s[8:9]
	v_mov_b32_e32 v131, v140
	v_mov_b32_e32 v140, v121
	v_mov_b32_e32 v177, v4
	v_add_f32_e32 v4, v114, v113
	v_mov_b32_e32 v10, v16
	v_mov_b32_e32 v11, v12
	v_mov_b32_e32 v130, v120
	v_pk_mul_f32 v[120:121], v[140:141], s[8:9]
	v_mov_b32_e32 v141, v142
	v_mov_b32_e32 v142, v15
	v_mov_b32_e32 v12, v17
	v_cvt_pk_f32_fp8_e32 v[16:17], v6
	v_cvt_pk_f32_fp8_e32 v[160:161], v2
	v_add_f32_e32 v4, v4, v66
	v_mov_b32_e32 v140, v14
	v_pk_mul_f32 v[14:15], v[142:143], s[8:9]
	v_mov_b32_e32 v143, v144
	v_mov_b32_e32 v144, v123
	v_add_f32_e32 v4, v4, v67
	v_mov_b32_e32 v142, v122
	v_pk_mul_f32 v[122:123], v[144:145], s[8:9]
	v_mov_b32_e32 v145, v146
	v_mov_b32_e32 v146, v125
	v_add_f32_e32 v4, v4, v132
	v_pk_mul_f32 v[150:151], v[150:151], s[8:9]
	v_mov_b32_e32 v144, v124
	v_pk_mul_f32 v[124:125], v[146:147], s[8:9]
	v_mov_b32_e32 v146, v126
	v_mov_b32_e32 v147, v148
	v_mov_b32_e32 v148, v127
	v_cvt_pk_f32_fp8_e32 v[154:155], v8
	v_cvt_pk_f32_fp8_sdwa v[156:157], v8 src0_sel:WORD_1
	v_cvt_pk_f32_fp8_e32 v[158:159], v9
	v_cvt_pk_f32_fp8_sdwa v[8:9], v9 src0_sel:WORD_1
	v_add_f32_e32 v4, v4, v133
	v_pk_mul_f32 v[10:11], v[10:11], s[8:9]
	v_pk_mul_f32 v[128:129], v[128:129], s[8:9]
	v_pk_mul_f32 v[130:131], v[130:131], s[8:9]
	v_pk_mul_f32 v[140:141], v[140:141], s[8:9]
	v_pk_mul_f32 v[142:143], v[142:143], s[8:9]
	v_pk_mul_f32 v[144:145], v[144:145], s[8:9]
	v_pk_mul_f32 v[146:147], v[146:147], s[8:9]
	v_pk_mul_f32 v[126:127], v[148:149], s[8:9]
	v_pk_mul_f32 v[12:13], v[12:13], s[8:9]
	v_readlane_b32 s8, v98, 6
	v_readlane_b32 s9, v98, 7
	v_mov_b32_e32 v178, v16
	v_mov_b32_e32 v179, v160
	v_add_f32_e32 v4, v4, v150
	v_pk_mul_f32 v[178:179], v[178:179], s[8:9]
	v_add_f32_e32 v4, v4, v151
	v_add_f32_e32 v4, v4, v178
	v_mov_b32_e32 v176, v8
	v_add_f32_e32 v8, v4, v179
	v_add_f32_e32 v4, v111, v112
	v_add_f32_e32 v4, v4, v62
	v_add_f32_e32 v4, v4, v63
	v_add_f32_e32 v4, v4, v134
	v_add_f32_e32 v4, v4, v135
	v_mov_b32_e32 v160, v17
	v_add_f32_e32 v4, v4, v116
	v_pk_mul_f32 v[16:17], v[160:161], s[8:9]
	v_add_f32_e32 v4, v4, v117
	v_add_f32_e32 v4, v4, v16
	v_add_f32_e32 v62, v4, v17
	v_add_f32_e32 v4, v110, v109
	v_cvt_pk_f32_fp8_sdwa v[148:149], v6 src0_sel:WORD_1
	v_cvt_pk_f32_fp8_sdwa v[164:165], v2 src0_sel:WORD_1
	v_add_f32_e32 v4, v4, v60
	v_add_f32_e32 v4, v4, v61
	v_add_f32_e32 v4, v4, v136
	v_add_f32_e32 v4, v4, v137
	v_mov_b32_e32 v16, v148
	v_mov_b32_e32 v17, v164
	v_add_f32_e32 v4, v4, v128
	v_pk_mul_f32 v[16:17], v[16:17], s[8:9]
	v_add_f32_e32 v4, v4, v129
	v_add_f32_e32 v4, v4, v16
	v_add_f32_e32 v60, v4, v17
	v_add_f32_e32 v4, v107, v108
; __device__ __forceinline__ unsigned pk2(float lo, float hi) { unsigned r; asm("v_cvt_pk_bf16_f32 %0, %1, %2" : "=v"(r) : "v"(lo), "v"(hi)); return r; }
; __device__ __forceinline__ void phase_combine(const Ptrs& P, int tid_, int vcu, int G) {
;     ...
;         for (int k = 0; k < 8; ++k) { const float g = __int_as_float(__builtin_amdgcn_readlane(__float_as_int(mg), k)); const unsigned w[4] = {yk[k].x, yk[k].y, yk[k].z, yk[k].w};
; #pragma unroll
;             for (int i = 0; i < 4; ++i) { const auto lo = __builtin_amdgcn_cvt_pk_f32_fp8((int)w[i], false); const auto hi = __builtin_amdgcn_cvt_pk_f32_fp8((int)w[i], true);
;                 v[4 * i] += g * lo[0]; v[4 * i + 1] += g * lo[1]; v[4 * i + 2] += g * hi[0]; v[4 * i + 3] += g * hi[1]; } }
;         v4u w0, w1; w0.x = pk2(v[0], v[1]); w0.y = pk2(v[2], v[3]); w0.z = pk2(v[4], v[5]); w0.w = pk2(v[6], v[7]); w1.x = pk2(v[8], v[9]); w1.y = pk2(v[10], v[11]); w1.z = pk2(v[12], v[13]); w1.w = pk2(v[14], v[15]);
;         v4u* hbo = (v4u*)(H + (size_t)t * D) + 2 * lane; hbo[0] = w0; hbo[1] = w1;
	v_add_f32_e32 v4, v4, v58
	v_add_f32_e32 v4, v4, v59
	v_add_f32_e32 v4, v4, v138
	v_add_f32_e32 v4, v4, v139
	v_mov_b32_e32 v164, v149
	v_add_f32_e32 v4, v4, v118
	v_pk_mul_f32 v[16:17], v[164:165], s[8:9]
	v_add_f32_e32 v4, v4, v119
	v_add_f32_e32 v4, v4, v16
	v_add_f32_e32 v58, v4, v17
	v_add_f32_e32 v4, v106, v105
	v_cvt_pk_f32_fp8_e32 v[152:153], v7
	v_cvt_pk_f32_fp8_e32 v[168:169], v3
	v_add_f32_e32 v4, v4, v56
	v_add_f32_e32 v4, v4, v57
	v_add_f32_e32 v4, v4, v80
	v_add_f32_e32 v4, v4, v81
	v_mov_b32_e32 v16, v152
	v_mov_b32_e32 v17, v168
	v_add_f32_e32 v4, v4, v130
	v_pk_mul_f32 v[16:17], v[16:17], s[8:9]
	v_add_f32_e32 v4, v4, v131
	v_add_f32_e32 v4, v4, v16
	v_add_f32_e32 v56, v4, v17
	v_add_f32_e32 v4, v103, v104
	v_add_f32_e32 v4, v4, v54
	v_add_f32_e32 v4, v4, v55
	v_add_f32_e32 v4, v4, v78
	v_cvt_pk_f32_fp8_sdwa v[2:3], v3 src0_sel:WORD_1
	v_add_f32_e32 v4, v4, v79
	v_mov_b32_e32 v168, v153
	v_add_f32_e32 v4, v4, v120
	v_pk_mul_f32 v[16:17], v[168:169], s[8:9]
	v_add_f32_e32 v4, v4, v121
	v_add_f32_e32 v4, v4, v16
	v_add_f32_e32 v54, v4, v17
	v_mov_b32_e32 v17, v2
	v_add_f32_e32 v2, v102, v101
	v_cvt_pk_f32_fp8_sdwa v[6:7], v7 src0_sel:WORD_1
	v_add_f32_e32 v2, v2, v52
	v_add_f32_e32 v2, v2, v53
	v_add_f32_e32 v2, v2, v76
	v_add_f32_e32 v4, v99, v100
	v_add_f32_e32 v2, v2, v77
	v_add_f32_e32 v4, v4, v50
	v_mov_b32_e32 v16, v6
	v_add_f32_e32 v2, v2, v140
	v_add_f32_e32 v4, v4, v51
	v_pk_mul_f32 v[16:17], v[16:17], s[8:9]
	v_add_f32_e32 v2, v2, v141
	v_add_f32_e32 v4, v4, v74
	v_add_f32_e32 v2, v2, v16
	v_add_f32_e32 v4, v4, v75
	v_add_f32_e32 v6, v2, v17
	v_mov_b32_e32 v2, v7
	v_add_f32_e32 v4, v4, v14
	v_pk_mul_f32 v[2:3], v[2:3], s[8:9]
	v_add_f32_e32 v4, v4, v15
	v_add_f32_e32 v2, v4, v2
	v_add_f32_e32 v4, v97, v96
	v_add_f32_e32 v4, v4, v48
	v_add_f32_e32 v4, v4, v49
	v_add_f32_e32 v4, v4, v72
	v_add_f32_e32 v4, v4, v73
	v_add_f32_e32 v7, v2, v3
	v_mov_b32_e32 v2, v154
	v_mov_b32_e32 v3, v170
	v_add_f32_e32 v4, v4, v142
	v_pk_mul_f32 v[2:3], v[2:3], s[8:9]
	v_add_f32_e32 v4, v4, v143
	v_add_f32_e32 v2, v4, v2
	v_add_f32_e32 v4, v94, v95
	v_add_f32_e32 v4, v4, v46
	v_add_f32_e32 v4, v4, v47
	v_add_f32_e32 v4, v4, v70
	v_add_f32_e32 v4, v4, v71
	v_mov_b32_e32 v170, v155
	v_add_f32_e32 v4, v4, v122
	v_add_f32_e32 v14, v2, v3
	v_pk_mul_f32 v[2:3], v[170:171], s[8:9]
	v_add_f32_e32 v4, v4, v123
	v_add_f32_e32 v2, v4, v2
	v_add_f32_e32 v4, v93, v92
	v_add_f32_e32 v4, v4, v44
	v_add_f32_e32 v4, v4, v45
	v_add_f32_e32 v4, v4, v68
	v_add_f32_e32 v4, v4, v69
	v_add_f32_e32 v15, v2, v3
	v_mov_b32_e32 v2, v156
	v_mov_b32_e32 v3, v172
	v_add_f32_e32 v4, v4, v144
	v_pk_mul_f32 v[2:3], v[2:3], s[8:9]
	v_add_f32_e32 v4, v4, v145
	v_add_f32_e32 v2, v4, v2
	v_add_f32_e32 v4, v90, v91
	v_add_f32_e32 v4, v4, v42
	v_add_f32_e32 v4, v4, v43
	v_add_f32_e32 v4, v4, v64
	v_add_f32_e32 v4, v4, v65
	v_mov_b32_e32 v172, v157
	v_add_f32_e32 v4, v4, v124
	v_add_f32_e32 v16, v2, v3
	v_pk_mul_f32 v[2:3], v[172:173], s[8:9]
	v_add_f32_e32 v4, v4, v125
	v_add_f32_e32 v2, v4, v2
	v_add_f32_e32 v4, v89, v88
	v_add_f32_e32 v4, v4, v40
	v_add_f32_e32 v4, v4, v41
	v_add_f32_e32 v4, v4, v24
	v_add_f32_e32 v4, v4, v25
	v_add_f32_e32 v17, v2, v3
	v_mov_b32_e32 v2, v158
	v_mov_b32_e32 v3, v174
	v_add_f32_e32 v4, v4, v146
	v_pk_mul_f32 v[2:3], v[2:3], s[8:9]
	v_add_f32_e32 v4, v4, v147
	v_add_f32_e32 v2, v4, v2
	v_add_f32_e32 v4, v86, v87
	v_add_f32_e32 v4, v4, v38
	v_add_f32_e32 v4, v4, v39
	v_add_f32_e32 v4, v4, v22
	v_add_f32_e32 v4, v4, v23
	v_mov_b32_e32 v174, v159
	v_add_f32_e32 v4, v4, v126
	v_add_f32_e32 v24, v2, v3
	v_pk_mul_f32 v[2:3], v[174:175], s[8:9]
	v_add_f32_e32 v4, v4, v127
	v_add_f32_e32 v2, v4, v2
	v_add_f32_e32 v22, v2, v3
	v_add_f32_e32 v2, v85, v84
	v_add_f32_e32 v2, v2, v26
	v_add_f32_e32 v2, v2, v27
	v_add_f32_e32 v2, v2, v18
	v_add_f32_e32 v2, v2, v19
	v_add_f32_e32 v2, v2, v10
	v_pk_mul_f32 v[176:177], v[176:177], s[8:9]
	v_add_f32_e32 v2, v2, v11
	v_add_f32_e32 v2, v2, v176
	v_mov_b32_e32 v4, v9
	v_add_f32_e32 v10, v2, v177
	v_pk_mul_f32 v[2:3], v[4:5], s[8:9]
	v_add_f32_e32 v4, v82, v83
	v_add_f32_e32 v4, v4, v28
	v_add_f32_e32 v4, v4, v29
	v_add_f32_e32 v4, v4, v20
	v_add_f32_e32 v4, v4, v21
	v_add_f32_e32 v4, v4, v12
	v_add_f32_e32 v4, v4, v13
	v_add_f32_e32 v2, v4, v2
	v_add_f32_e32 v9, v2, v3
	v_cvt_pk_bf16_f32 v2, v8, v62
	v_cvt_pk_bf16_f32 v3, v60, v58
	v_cvt_pk_bf16_f32 v4, v56, v54
	v_cvt_pk_bf16_f32 v5, v6, v7
	v_cvt_pk_bf16_f32 v6, v14, v15
	v_cvt_pk_bf16_f32 v7, v16, v17
	v_cvt_pk_bf16_f32 v8, v24, v22
	v_cvt_pk_bf16_f32 v9, v10, v9
	global_store_dwordx4 v[36:37], v[2:5], off
	global_store_dwordx4 v[36:37], v[6:9], off offset:16
	s_andn2_b64 exec, exec, s[12:13]
	s_cbranch_execz .LBB0_1444
; __device__ __forceinline__ float bflo(unsigned w) { return __uint_as_float(w << 16); }
; __device__ __forceinline__ float bfhi(unsigned w) { return __uint_as_float(w & 0xffff0000u); }
; __device__ __forceinline__ void phase_combine(const Ptrs& P, int tid_, int vcu, int G) {
;     ...
;     for (int t = gw; t < T; t += NGW) {
;         float v[16]; v4u ys[2], yk[8];
;         const v4u* hp = (const v4u*)(H + (size_t)t * D) + 2 * lane; const v4u* ysp = (const v4u*)(YS + (size_t)t * D) + 2 * lane; const v4u* yr = (const v4u*)(Y8 + (size_t)t * 8 * 1024) + lane;
;         float mg = 0.f; if (lane < 8) mg = tg[(size_t)t * 8 + lane] * (1.f / 16.f);
; #pragma unroll
;         for (int q = 0; q < 2; ++q) { const v4u a = hp[q]; v[8 * q] = bflo(a.x); v[8 * q + 1] = bfhi(a.x); v[8 * q + 2] = bflo(a.y); v[8 * q + 3] = bfhi(a.y); v[8 * q + 4] = bflo(a.z); v[8 * q + 5] = bfhi(a.z); v[8 * q + 6] = bflo(a.w); v[8 * q + 7] = bfhi(a.w); }
;         ys[0] = __builtin_nontemporal_load(ysp); ys[1] = __builtin_nontemporal_load(ysp + 1);
; #pragma unroll
;         for (int k = 0; k < 8; ++k) yk[k] = __builtin_nontemporal_load(yr + k * 64);
.LBB0_1442:
	s_waitcnt vmcnt(2)
	v_lshl_add_u64 v[2:3], s[6:7], 0, v[34:35]
	v_add_co_u32_e32 v36, vcc, 0x34600000, v2
	s_nop 1
	v_addc_co_u32_e32 v37, vcc, 0, v3, vcc
	v_mov_b64_e32 v[38:39], v[180:181]
	v_mov_b64_e32 v[40:41], v[182:183]
	v_mov_b64_e32 v[42:43], v[184:185]
	v_mov_b64_e32 v[44:45], v[186:187]
	v_mov_b64_e32 v[46:47], v[188:189]
	v_mov_b64_e32 v[48:49], v[190:191]
	v_mov_b64_e32 v[50:51], v[192:193]
	v_mov_b64_e32 v[52:53], v[194:195]
	v_mov_b64_e32 v[54:55], v[200:201]
	v_mov_b64_e32 v[56:57], v[202:203]
	v_mov_b64_e32 v[26:27], v[204:205]
	v_mov_b64_e32 v[28:29], v[206:207]
	v_mov_b64_e32 v[22:23], v[208:209]
	v_mov_b64_e32 v[24:25], v[210:211]
	v_mov_b64_e32 v[18:19], v[212:213]
	v_mov_b64_e32 v[20:21], v[214:215]
	v_mov_b64_e32 v[14:15], v[216:217]
	v_mov_b64_e32 v[16:17], v[218:219]
	v_mov_b64_e32 v[10:11], v[220:221]
	v_mov_b64_e32 v[12:13], v[222:223]
	v_mov_b64_e32 v[6:7], v[224:225]
	v_mov_b64_e32 v[8:9], v[226:227]
	v_mov_b64_e32 v[2:3], v[228:229]
	v_mov_b64_e32 v[4:5], v[230:231]
	v_mul_f32_e32 v98, 0x3d800000, v232
	v_mov_b64_e32 v[234:235], v[30:31]
	v_mov_b64_e32 v[236:237], v[32:33]
	v_mov_b64_e32 v[238:239], v[34:35]
	v_readlane_b32 s4, v255, 52
	v_readlane_b32 s5, v255, 53
	v_add_u32_e32 v1, s74, v1
	v_cmp_lt_i32_e32 vcc, s10, v1
	v_lshl_add_u64 v[30:31], v[30:31], 0, s[4:5]
	v_readlane_b32 s4, v255, 54
	v_readlane_b32 s5, v255, 55
	v_lshl_add_u64 v[34:35], v[34:35], 0, s[94:95]
	s_or_b64 s[12:13], vcc, s[12:13]
	v_lshl_add_u64 v[32:33], v[32:33], 0, s[4:5]
	v_cndmask_b32_e32 v234, v30, v234, vcc
	v_cndmask_b32_e32 v235, v31, v235, vcc
	v_cndmask_b32_e32 v236, v32, v236, vcc
	v_cndmask_b32_e32 v237, v33, v237, vcc
	v_cndmask_b32_e32 v238, v34, v238, vcc
	v_cndmask_b32_e32 v239, v35, v239, vcc
	s_and_saveexec_b64 s[8:9], s[38:39]
	v_lshl_add_u64 v[240:241], s[6:7], 0, v[234:235]
	global_load_dword v232, v[240:241], off
	s_or_b64 exec, exec, s[8:9]
	v_lshl_add_u64 v[240:241], s[6:7], 0, v[238:239]
	v_add_co_u32_e32 v242, vcc, 0x34600000, v240
	s_nop 1
	v_addc_co_u32_e32 v243, vcc, 0, v241, vcc
	global_load_dwordx4 v[180:183], v[242:243], off
	global_load_dwordx4 v[184:187], v[242:243], off offset:16
	v_add_co_u32_e32 v242, vcc, 0x3a600000, v240
	s_nop 1
	v_addc_co_u32_e32 v243, vcc, 0, v241, vcc
	global_load_dwordx4 v[188:191], v[242:243], off nt
	global_load_dwordx4 v[192:195], v[242:243], off offset:16 nt
	v_lshl_add_u64 v[240:241], s[6:7], 0, v[236:237]
	v_add_co_u32_e32 v242, vcc, 0x3c600000, v240
	s_nop 1
	v_addc_co_u32_e32 v243, vcc, 0, v241, vcc
	global_load_dwordx4 v[200:203], v[242:243], off nt
	global_load_dwordx4 v[204:207], v[242:243], off offset:1024 nt
	global_load_dwordx4 v[208:211], v[242:243], off offset:2048 nt
	global_load_dwordx4 v[212:215], v[242:243], off offset:3072 nt
	v_add_co_u32_e32 v242, vcc, 0x3c601000, v240
	s_nop 1
	v_addc_co_u32_e32 v243, vcc, 0, v241, vcc
	global_load_dwordx4 v[216:219], v[242:243], off nt
	global_load_dwordx4 v[220:223], v[242:243], off offset:1024 nt
	global_load_dwordx4 v[224:227], v[242:243], off offset:2048 nt
	global_load_dwordx4 v[228:231], v[242:243], off offset:3072 nt
	v_readlane_b32 s8, v98, 0
	v_readlane_b32 s9, v98, 1
	s_branch .Lcomb_body
